# edown tile body rewritten as 32-step software pipeline (ring of 4 LDS half-slabs, rolling B-fragment prefetch, epilogue interleaved under next step MFMAs)
# speedup vs baseline: 1.0068x; 1.0068x over previous
; #define GAS __attribute__((address_space(1)))
; #define D2_STAGE(slot, J) do { _Pragma("unroll") for (int _h = 0; _h < 2; ++_h) _Pragma("unroll") for (int _i = 0; _i < 2; ++_i) \
;         __builtin_amdgcn_global_load_lds((const unsigned*)(wd + (size_t)(2 * (J) + _h) * (32 * 512) + goff[_i]), (LAS unsigned*)(c.lds + (slot) * 32768 + _h * 16384 + ldsw + _i * 8192), 16, 0, 0); } while (0)
; DI void phase_edown3(const Ctx& c, int layer) {
;     ...
;         if (wid == 0) {
;             unsigned sp = 0u;
;             while (fv < 2u) { fv = __hip_atomic_load(flags + (orow >> 8), __ATOMIC_RELAXED, __HIP_MEMORY_SCOPE_AGENT); if (fv >= 2u || ++sp > (1u << 18)) break; __builtin_amdgcn_s_sleep(8); }
;             __builtin_amdgcn_fence(__ATOMIC_ACQUIRE, "agent");
;             asm volatile("s_waitcnt vmcnt(0)" ::: "memory");
;         }
;         asm volatile("s_waitcnt lgkmcnt(0)" ::: "memory"); __builtin_amdgcn_s_barrier(); asm volatile("" ::: "memory");
;         bf16x8 afr[2][8];
; #pragma unroll
;         for (int mb = 0; mb < 2; ++mb)
; #pragma unroll
;             for (int ks = 0; ks < 8; ++ks) afr[mb][ks] = *(const GAS bf16x8*)(ACT + (size_t)(orow + 32 * wid + 16 * mb + fr) * 256 + ks * 32 + fq * 8);
;         if (wid == 0) {
;             const int pn2 = p + 256; fv = 0u;
;             if (pn2 < ntiles) { int tn; if (pn2 < 720) tn = (pn2 / 80) * 128 + 48 + pn2 % 80; else { const int q = pn2 - 720; tn = (q < 432) ? (q / 48) * 128 + q % 48 : 1152 + (q - 432); }
;                 fv = __hip_atomic_load(flags + (tn < nrt ? tn : (SH_BASE >> 8) + (tn - nrt)), __ATOMIC_RELAXED, __HIP_MEMORY_SCOPE_AGENT); }
;         }
;         D2_STAGE(0, 0);
;         bf16x8 bfr[8][2];
;         f32x4 acc[2][2];
; #pragma unroll
;         for (int mb = 0; mb < 2; ++mb)
; #pragma unroll
;             for (int nb = 0; nb < 2; ++nb) acc[mb][nb] = (f32x4){0.f, 0.f, 0.f, 0.f};
.LBB0_1282:
	s_mov_b32 m0, s30
	s_nop 0
	global_load_lds_dwordx4 v176, s[16:17]
	s_add_i32 m0, s30, 0x2000
	s_nop 0
	global_load_lds_dwordx4 v64, s[16:17]
	s_add_u32 s16, s16, 0x4000
	s_addc_u32 s17, s17, 0
	s_add_i32 m0, s30, 0x4000
	s_nop 0
	global_load_lds_dwordx4 v176, s[16:17]
	s_add_i32 m0, s30, 0x6000
	s_nop 0
	global_load_lds_dwordx4 v64, s[16:17]
	s_add_u32 s16, s16, 0x4000
	s_addc_u32 s17, s17, 0
	s_add_i32 m0, s30, 0x8000
	s_nop 0
	global_load_lds_dwordx4 v176, s[16:17]
	s_add_i32 m0, s30, 0xa000
	s_nop 0
	global_load_lds_dwordx4 v64, s[16:17]
	s_add_u32 s16, s16, 0x4000
	s_addc_u32 s17, s17, 0
	v_add_u32_e32 v106, v89, v86
	v_add_u32_e32 v107, 32, v102
	v_add_u32_e32 v108, 64, v102
	v_add_u32_e32 v109, 0x60, v102
	s_add_i32 s6, s40, s29
	v_mbcnt_lo_u32_b32 v111, -1, 0
	v_mbcnt_hi_u32_b32 v111, -1, v111
	v_add_u32_e32 v72, s6, v90
	v_and_b32_e32 v73, 7, v111
	v_lshlrev_b32_e32 v73, 4, v73
	v_mad_u32_u24 v72, v72, s50, v73
	v_add_u32_e32 v76, s6, v111
	v_mul_u32_u24_e32 v76, s50, v76
	v_add_u32_e32 v73, 0x2400, v72
	v_add_u32_e32 v74, 0x4800, v72
	v_add_u32_e32 v75, 0x6c00, v72
	v_add_u32_e32 v76, 0x400, v76
	s_waitcnt vmcnt(4)
	s_barrier
	ds_read_b128 v[112:115], v94
	ds_read_b128 v[116:119], v94 offset:8192
	ds_read_b128 v[120:123], v95
	ds_read_b128 v[124:127], v95 offset:8192
	ds_read_b128 v[128:131], v96
	ds_read_b128 v[132:135], v96 offset:8192
	ds_read_b128 v[136:139], v97
	ds_read_b128 v[140:143], v97 offset:8192
	ds_read_b128 v[144:147], v98
	ds_read_b128 v[148:151], v98 offset:8192
	ds_read_b128 v[152:155], v99
	ds_read_b128 v[156:159], v99 offset:8192
	ds_read_b128 v[210:213], v100
	ds_read_b128 v[214:217], v100 offset:8192
	ds_read_b128 v[236:239], v101
	ds_read_b128 v[240:243], v101 offset:8192
	s_waitcnt vmcnt(2) lgkmcnt(0)
	s_barrier
	s_add_i32 m0, s30, 0xc000
	s_nop 0
	global_load_lds_dwordx4 v176, s[16:17]
	s_add_i32 m0, s30, 0xe000
	s_nop 0
	global_load_lds_dwordx4 v64, s[16:17]
	s_add_u32 s16, s16, 0x4000
	s_addc_u32 s17, s17, 0
	v_mfma_f32_16x16x32_bf16 v[178:181], v[112:115], v[0:3], 0
	v_mfma_f32_16x16x32_bf16 v[182:185], v[116:119], v[0:3], 0
	ds_read_b128 v[160:163], v100 offset:16384
	ds_read_b128 v[164:167], v100 offset:24576
	v_mfma_f32_16x16x32_bf16 v[186:189], v[112:115], v[32:35], 0
	v_mfma_f32_16x16x32_bf16 v[190:193], v[116:119], v[32:35], 0
	ds_read_b128 v[168:171], v101 offset:16384
	ds_read_b128 v[172:175], v101 offset:24576
	v_mfma_f32_16x16x32_bf16 v[178:181], v[120:123], v[4:7], v[178:181]
	v_mfma_f32_16x16x32_bf16 v[182:185], v[124:127], v[4:7], v[182:185]
	v_mfma_f32_16x16x32_bf16 v[186:189], v[120:123], v[36:39], v[186:189]
	v_mfma_f32_16x16x32_bf16 v[190:193], v[124:127], v[36:39], v[190:193]
	ds_read_b128 v[112:115], v94 offset:16384
	ds_read_b128 v[116:119], v94 offset:24576
	v_mfma_f32_16x16x32_bf16 v[178:181], v[128:131], v[8:11], v[178:181]
	v_mfma_f32_16x16x32_bf16 v[182:185], v[132:135], v[8:11], v[182:185]
	v_mfma_f32_16x16x32_bf16 v[186:189], v[128:131], v[40:43], v[186:189]
	v_mfma_f32_16x16x32_bf16 v[190:193], v[132:135], v[40:43], v[190:193]
	ds_read_b128 v[120:123], v95 offset:16384
	ds_read_b128 v[124:127], v95 offset:24576
	v_mfma_f32_16x16x32_bf16 v[178:181], v[136:139], v[12:15], v[178:181]
	v_mfma_f32_16x16x32_bf16 v[182:185], v[140:143], v[12:15], v[182:185]
	v_mfma_f32_16x16x32_bf16 v[186:189], v[136:139], v[44:47], v[186:189]
	v_mfma_f32_16x16x32_bf16 v[190:193], v[140:143], v[44:47], v[190:193]
	ds_read_b128 v[128:131], v96 offset:16384
	ds_read_b128 v[132:135], v96 offset:24576
	v_mfma_f32_16x16x32_bf16 v[178:181], v[144:147], v[16:19], v[178:181]
	v_mfma_f32_16x16x32_bf16 v[182:185], v[148:151], v[16:19], v[182:185]
	v_mfma_f32_16x16x32_bf16 v[186:189], v[144:147], v[48:51], v[186:189]
	v_mfma_f32_16x16x32_bf16 v[190:193], v[148:151], v[48:51], v[190:193]
	ds_read_b128 v[136:139], v97 offset:16384
	ds_read_b128 v[140:143], v97 offset:24576
	v_mfma_f32_16x16x32_bf16 v[178:181], v[152:155], v[20:23], v[178:181]
	v_mfma_f32_16x16x32_bf16 v[182:185], v[156:159], v[20:23], v[182:185]
	v_mfma_f32_16x16x32_bf16 v[186:189], v[152:155], v[52:55], v[186:189]
	v_mfma_f32_16x16x32_bf16 v[190:193], v[156:159], v[52:55], v[190:193]
	ds_read_b128 v[144:147], v98 offset:16384
	ds_read_b128 v[148:151], v98 offset:24576
	v_mfma_f32_16x16x32_bf16 v[178:181], v[210:213], v[24:27], v[178:181]
	v_mfma_f32_16x16x32_bf16 v[182:185], v[214:217], v[24:27], v[182:185]
	v_mfma_f32_16x16x32_bf16 v[186:189], v[210:213], v[56:59], v[186:189]
	v_mfma_f32_16x16x32_bf16 v[190:193], v[214:217], v[56:59], v[190:193]
	ds_read_b128 v[152:155], v99 offset:16384
	ds_read_b128 v[156:159], v99 offset:24576
	v_mfma_f32_16x16x32_bf16 v[178:181], v[236:239], v[28:31], v[178:181]
	v_mfma_f32_16x16x32_bf16 v[182:185], v[240:243], v[28:31], v[182:185]
	v_mfma_f32_16x16x32_bf16 v[186:189], v[236:239], v[60:63], v[186:189]
	v_mfma_f32_16x16x32_bf16 v[190:193], v[240:243], v[60:63], v[190:193]
	s_waitcnt vmcnt(2) lgkmcnt(0)
	s_barrier
	s_mov_b32 m0, s30
	s_nop 0
	global_load_lds_dwordx4 v176, s[16:17]
	s_add_i32 m0, s30, 0x2000
	s_nop 0
	global_load_lds_dwordx4 v64, s[16:17]
	s_add_u32 s16, s16, 0x4000
	s_addc_u32 s17, s17, 0
	v_mfma_f32_16x16x32_bf16 v[194:197], v[112:115], v[0:3], 0
	v_mfma_f32_16x16x32_bf16 v[198:201], v[116:119], v[0:3], 0
	ds_read_b128 v[210:213], v100 offset:32768
	ds_read_b128 v[214:217], v100 offset:40960
	v_mfma_f32_16x16x32_bf16 v[202:205], v[112:115], v[32:35], 0
	v_mfma_f32_16x16x32_bf16 v[206:209], v[116:119], v[32:35], 0
	ds_read_b128 v[236:239], v101 offset:32768
	ds_read_b128 v[240:243], v101 offset:40960
	v_max3_f32 v77, |v178|, |v179|, |v180|
	v_max3_f32 v84, |v186|, |v187|, |v188|
	v_mfma_f32_16x16x32_bf16 v[194:197], v[120:123], v[4:7], v[194:197]
	v_max3_f32 v78, |v181|, |v182|, |v183|
	v_max3_f32 v85, |v189|, |v190|, |v191|
	v_mfma_f32_16x16x32_bf16 v[198:201], v[124:127], v[4:7], v[198:201]
	v_max3_f32 v77, |v184|, |v185|, v77
	v_max3_f32 v84, |v192|, |v193|, v84
	v_mfma_f32_16x16x32_bf16 v[202:205], v[120:123], v[36:39], v[202:205]
	v_max_f32_e32 v77, v77, v78
	v_max_f32_e32 v84, v84, v85
	v_mfma_f32_16x16x32_bf16 v[206:209], v[124:127], v[36:39], v[206:209]
	ds_read_b128 v[112:115], v94 offset:32768
	ds_read_b128 v[116:119], v94 offset:40960
	v_mul_f32_e32 v77, 0x3c010204, v77
	v_mul_f32_e32 v84, 0x3c010204, v84
	v_mfma_f32_16x16x32_bf16 v[194:197], v[128:131], v[8:11], v[194:197]
	v_lshrrev_b32_e32 v79, 23, v77
	v_lshrrev_b32_e32 v110, 23, v84
	v_mfma_f32_16x16x32_bf16 v[198:201], v[132:135], v[8:11], v[198:201]
	v_and_b32_e32 v77, 0x7f800000, v77
	v_and_b32_e32 v84, 0x7f800000, v84
	v_mfma_f32_16x16x32_bf16 v[202:205], v[128:131], v[40:43], v[202:205]
	v_sub_u32_e32 v77, 0x7e800000, v77
	v_sub_u32_e32 v84, 0x7e800000, v84
	v_mfma_f32_16x16x32_bf16 v[206:209], v[132:135], v[40:43], v[206:209]
	ds_read_b128 v[120:123], v95 offset:32768
	ds_read_b128 v[124:127], v95 offset:40960
	v_fmaak_f32 v78, v178, v77, 0x43000000
	v_fmaak_f32 v85, v186, v84, 0x43000000
	v_mfma_f32_16x16x32_bf16 v[194:197], v[136:139], v[12:15], v[194:197]
	v_cvt_pk_u8_f32 v80, v78, 0, 0
	v_cvt_pk_u8_f32 v82, v85, 0, 0
	v_mfma_f32_16x16x32_bf16 v[198:201], v[140:143], v[12:15], v[198:201]
	v_fmaak_f32 v78, v179, v77, 0x43000000
	v_fmaak_f32 v85, v187, v84, 0x43000000
	v_mfma_f32_16x16x32_bf16 v[202:205], v[136:139], v[44:47], v[202:205]
	v_cvt_pk_u8_f32 v80, v78, 1, v80
	v_cvt_pk_u8_f32 v82, v85, 1, v82
	v_mfma_f32_16x16x32_bf16 v[206:209], v[140:143], v[44:47], v[206:209]
	ds_read_b128 v[128:131], v96 offset:32768
	ds_read_b128 v[132:135], v96 offset:40960
	v_fmaak_f32 v78, v180, v77, 0x43000000
	v_fmaak_f32 v85, v188, v84, 0x43000000
	v_mfma_f32_16x16x32_bf16 v[194:197], v[144:147], v[16:19], v[194:197]
	v_cvt_pk_u8_f32 v80, v78, 2, v80
	v_cvt_pk_u8_f32 v82, v85, 2, v82
	v_mfma_f32_16x16x32_bf16 v[198:201], v[148:151], v[16:19], v[198:201]
	v_fmaak_f32 v78, v181, v77, 0x43000000
	v_fmaak_f32 v85, v189, v84, 0x43000000
	v_mfma_f32_16x16x32_bf16 v[202:205], v[144:147], v[48:51], v[202:205]
	v_cvt_pk_u8_f32 v80, v78, 3, v80
	v_cvt_pk_u8_f32 v82, v85, 3, v82
	v_mfma_f32_16x16x32_bf16 v[206:209], v[148:151], v[48:51], v[206:209]
	ds_read_b128 v[136:139], v97 offset:32768
	ds_read_b128 v[140:143], v97 offset:40960
	v_fmaak_f32 v78, v182, v77, 0x43000000
	v_fmaak_f32 v85, v190, v84, 0x43000000
	v_mfma_f32_16x16x32_bf16 v[194:197], v[152:155], v[20:23], v[194:197]
	v_cvt_pk_u8_f32 v81, v78, 0, 0
	v_cvt_pk_u8_f32 v83, v85, 0, 0
	v_mfma_f32_16x16x32_bf16 v[198:201], v[156:159], v[20:23], v[198:201]
	v_fmaak_f32 v78, v183, v77, 0x43000000
	v_fmaak_f32 v85, v191, v84, 0x43000000
	v_mfma_f32_16x16x32_bf16 v[202:205], v[152:155], v[52:55], v[202:205]
	v_cvt_pk_u8_f32 v81, v78, 1, v81
	v_cvt_pk_u8_f32 v83, v85, 1, v83
	v_mfma_f32_16x16x32_bf16 v[206:209], v[156:159], v[52:55], v[206:209]
	ds_read_b128 v[144:147], v98 offset:32768
	ds_read_b128 v[148:151], v98 offset:40960
	v_fmaak_f32 v78, v184, v77, 0x43000000
	v_fmaak_f32 v85, v192, v84, 0x43000000
	v_mfma_f32_16x16x32_bf16 v[194:197], v[160:163], v[24:27], v[194:197]
	v_cvt_pk_u8_f32 v81, v78, 2, v81
	v_cvt_pk_u8_f32 v83, v85, 2, v83
	v_mfma_f32_16x16x32_bf16 v[198:201], v[164:167], v[24:27], v[198:201]
	v_fmaak_f32 v78, v185, v77, 0x43000000
	v_fmaak_f32 v85, v193, v84, 0x43000000
	v_mfma_f32_16x16x32_bf16 v[202:205], v[160:163], v[56:59], v[202:205]
	v_cvt_pk_u8_f32 v81, v78, 3, v81
	v_cvt_pk_u8_f32 v83, v85, 3, v83
	v_mfma_f32_16x16x32_bf16 v[206:209], v[164:167], v[56:59], v[206:209]
	ds_read_b128 v[152:155], v99 offset:32768
	ds_read_b128 v[156:159], v99 offset:40960
	v_add_u16_e32 v79, 1, v79
	v_add_u16_e32 v110, 1, v110
	v_mfma_f32_16x16x32_bf16 v[194:197], v[168:171], v[28:31], v[194:197]
	ds_write_b8 v106, v79 offset:128
	ds_write_b8 v106, v110 offset:2688
	v_mfma_f32_16x16x32_bf16 v[198:201], v[172:175], v[28:31], v[198:201]
	ds_write2st64_b64 v102, v[80:81], v[82:83] offset1:5
	v_mfma_f32_16x16x32_bf16 v[202:205], v[168:171], v[60:63], v[202:205]
	v_mfma_f32_16x16x32_bf16 v[206:209], v[172:175], v[60:63], v[206:209]
	s_waitcnt vmcnt(2) lgkmcnt(0)
	s_barrier
	s_add_i32 m0, s30, 0x4000
	s_nop 0
	global_load_lds_dwordx4 v176, s[16:17]
	s_add_i32 m0, s30, 0x6000
	s_nop 0
	global_load_lds_dwordx4 v64, s[16:17]
	s_add_u32 s16, s16, 0x4000
	s_addc_u32 s17, s17, 0
	v_mfma_f32_16x16x32_bf16 v[178:181], v[112:115], v[0:3], 0
	v_mfma_f32_16x16x32_bf16 v[182:185], v[116:119], v[0:3], 0
	ds_read_b128 v[160:163], v100 offset:49152
	ds_read_b128 v[164:167], v100 offset:57344
	v_mfma_f32_16x16x32_bf16 v[186:189], v[112:115], v[32:35], 0
	v_mfma_f32_16x16x32_bf16 v[190:193], v[116:119], v[32:35], 0
	ds_read_b128 v[168:171], v101 offset:49152
	ds_read_b128 v[172:175], v101 offset:57344
	v_max3_f32 v77, |v194|, |v195|, |v196|
	v_max3_f32 v84, |v202|, |v203|, |v204|
	v_mfma_f32_16x16x32_bf16 v[178:181], v[120:123], v[4:7], v[178:181]
	v_max3_f32 v78, |v197|, |v198|, |v199|
	v_max3_f32 v85, |v205|, |v206|, |v207|
	v_mfma_f32_16x16x32_bf16 v[182:185], v[124:127], v[4:7], v[182:185]
	v_max3_f32 v77, |v200|, |v201|, v77
	v_max3_f32 v84, |v208|, |v209|, v84
	v_mfma_f32_16x16x32_bf16 v[186:189], v[120:123], v[36:39], v[186:189]
	v_max_f32_e32 v77, v77, v78
	v_max_f32_e32 v84, v84, v85
	v_mfma_f32_16x16x32_bf16 v[190:193], v[124:127], v[36:39], v[190:193]
	ds_read_b128 v[112:115], v94 offset:49152
	ds_read_b128 v[116:119], v94 offset:57344
	v_mul_f32_e32 v77, 0x3c010204, v77
	v_mul_f32_e32 v84, 0x3c010204, v84
	v_mfma_f32_16x16x32_bf16 v[178:181], v[128:131], v[8:11], v[178:181]
	v_lshrrev_b32_e32 v79, 23, v77
	v_lshrrev_b32_e32 v110, 23, v84
	v_mfma_f32_16x16x32_bf16 v[182:185], v[132:135], v[8:11], v[182:185]
	v_and_b32_e32 v77, 0x7f800000, v77
	v_and_b32_e32 v84, 0x7f800000, v84
	v_mfma_f32_16x16x32_bf16 v[186:189], v[128:131], v[40:43], v[186:189]
	v_sub_u32_e32 v77, 0x7e800000, v77
	v_sub_u32_e32 v84, 0x7e800000, v84
	v_mfma_f32_16x16x32_bf16 v[190:193], v[132:135], v[40:43], v[190:193]
	ds_read_b128 v[120:123], v95 offset:49152
	ds_read_b128 v[124:127], v95 offset:57344
	v_fmaak_f32 v78, v194, v77, 0x43000000
	v_fmaak_f32 v85, v202, v84, 0x43000000
	v_mfma_f32_16x16x32_bf16 v[178:181], v[136:139], v[12:15], v[178:181]
	v_cvt_pk_u8_f32 v80, v78, 0, 0
	v_cvt_pk_u8_f32 v82, v85, 0, 0
	v_mfma_f32_16x16x32_bf16 v[182:185], v[140:143], v[12:15], v[182:185]
	v_fmaak_f32 v78, v195, v77, 0x43000000
	v_fmaak_f32 v85, v203, v84, 0x43000000
	v_mfma_f32_16x16x32_bf16 v[186:189], v[136:139], v[44:47], v[186:189]
	v_cvt_pk_u8_f32 v80, v78, 1, v80
	v_cvt_pk_u8_f32 v82, v85, 1, v82
	v_mfma_f32_16x16x32_bf16 v[190:193], v[140:143], v[44:47], v[190:193]
	ds_read_b128 v[128:131], v96 offset:49152
	ds_read_b128 v[132:135], v96 offset:57344
	v_fmaak_f32 v78, v196, v77, 0x43000000
	v_fmaak_f32 v85, v204, v84, 0x43000000
	v_mfma_f32_16x16x32_bf16 v[178:181], v[144:147], v[16:19], v[178:181]
	v_cvt_pk_u8_f32 v80, v78, 2, v80
	v_cvt_pk_u8_f32 v82, v85, 2, v82
	v_mfma_f32_16x16x32_bf16 v[182:185], v[148:151], v[16:19], v[182:185]
	v_fmaak_f32 v78, v197, v77, 0x43000000
	v_fmaak_f32 v85, v205, v84, 0x43000000
	v_mfma_f32_16x16x32_bf16 v[186:189], v[144:147], v[48:51], v[186:189]
	v_cvt_pk_u8_f32 v80, v78, 3, v80
	v_cvt_pk_u8_f32 v82, v85, 3, v82
	v_mfma_f32_16x16x32_bf16 v[190:193], v[148:151], v[48:51], v[190:193]
	ds_read_b128 v[136:139], v97 offset:49152
	ds_read_b128 v[140:143], v97 offset:57344
	v_fmaak_f32 v78, v198, v77, 0x43000000
	v_fmaak_f32 v85, v206, v84, 0x43000000
	v_mfma_f32_16x16x32_bf16 v[178:181], v[152:155], v[20:23], v[178:181]
	v_cvt_pk_u8_f32 v81, v78, 0, 0
	v_cvt_pk_u8_f32 v83, v85, 0, 0
	v_mfma_f32_16x16x32_bf16 v[182:185], v[156:159], v[20:23], v[182:185]
	v_fmaak_f32 v78, v199, v77, 0x43000000
	v_fmaak_f32 v85, v207, v84, 0x43000000
	v_mfma_f32_16x16x32_bf16 v[186:189], v[152:155], v[52:55], v[186:189]
	v_cvt_pk_u8_f32 v81, v78, 1, v81
	v_cvt_pk_u8_f32 v83, v85, 1, v83
	v_mfma_f32_16x16x32_bf16 v[190:193], v[156:159], v[52:55], v[190:193]
	ds_read_b128 v[144:147], v98 offset:49152
	ds_read_b128 v[148:151], v98 offset:57344
	v_fmaak_f32 v78, v200, v77, 0x43000000
	v_fmaak_f32 v85, v208, v84, 0x43000000
	v_mfma_f32_16x16x32_bf16 v[178:181], v[210:213], v[24:27], v[178:181]
	v_cvt_pk_u8_f32 v81, v78, 2, v81
	v_cvt_pk_u8_f32 v83, v85, 2, v83
	v_mfma_f32_16x16x32_bf16 v[182:185], v[214:217], v[24:27], v[182:185]
	v_fmaak_f32 v78, v201, v77, 0x43000000
	v_fmaak_f32 v85, v209, v84, 0x43000000
	v_mfma_f32_16x16x32_bf16 v[186:189], v[210:213], v[56:59], v[186:189]
	v_cvt_pk_u8_f32 v81, v78, 3, v81
	v_cvt_pk_u8_f32 v83, v85, 3, v83
	v_mfma_f32_16x16x32_bf16 v[190:193], v[214:217], v[56:59], v[190:193]
	ds_read_b128 v[152:155], v99 offset:49152
	ds_read_b128 v[156:159], v99 offset:57344
	v_add_u16_e32 v79, 1, v79
	v_add_u16_e32 v110, 1, v110
	v_mfma_f32_16x16x32_bf16 v[178:181], v[236:239], v[28:31], v[178:181]
	ds_write_b8 v106, v79 offset:132
	ds_write_b8 v106, v110 offset:2692
	v_mfma_f32_16x16x32_bf16 v[182:185], v[240:243], v[28:31], v[182:185]
	ds_write2st64_b64 v107, v[80:81], v[82:83] offset1:5
	v_mfma_f32_16x16x32_bf16 v[186:189], v[236:239], v[60:63], v[186:189]
	v_mfma_f32_16x16x32_bf16 v[190:193], v[240:243], v[60:63], v[190:193]
	s_waitcnt vmcnt(2) lgkmcnt(0)
	s_barrier
	s_add_i32 m0, s30, 0x8000
	s_nop 0
	global_load_lds_dwordx4 v176, s[16:17]
	s_add_i32 m0, s30, 0xa000
	s_nop 0
	global_load_lds_dwordx4 v64, s[16:17]
	s_add_u32 s16, s16, 0x4000
	s_addc_u32 s17, s17, 0
	v_mfma_f32_16x16x32_bf16 v[194:197], v[112:115], v[0:3], 0
	v_mfma_f32_16x16x32_bf16 v[198:201], v[116:119], v[0:3], 0
	ds_read_b128 v[210:213], v100
	ds_read_b128 v[214:217], v100 offset:8192
	v_mfma_f32_16x16x32_bf16 v[202:205], v[112:115], v[32:35], 0
	v_mfma_f32_16x16x32_bf16 v[206:209], v[116:119], v[32:35], 0
	ds_read_b128 v[236:239], v101
	ds_read_b128 v[240:243], v101 offset:8192
	v_max3_f32 v77, |v178|, |v179|, |v180|
	v_max3_f32 v84, |v186|, |v187|, |v188|
	v_mfma_f32_16x16x32_bf16 v[194:197], v[120:123], v[4:7], v[194:197]
	v_max3_f32 v78, |v181|, |v182|, |v183|
	v_max3_f32 v85, |v189|, |v190|, |v191|
	v_mfma_f32_16x16x32_bf16 v[198:201], v[124:127], v[4:7], v[198:201]
	v_max3_f32 v77, |v184|, |v185|, v77
	v_max3_f32 v84, |v192|, |v193|, v84
	v_mfma_f32_16x16x32_bf16 v[202:205], v[120:123], v[36:39], v[202:205]
	v_max_f32_e32 v77, v77, v78
	v_max_f32_e32 v84, v84, v85
	v_mfma_f32_16x16x32_bf16 v[206:209], v[124:127], v[36:39], v[206:209]
	ds_read_b128 v[112:115], v94
	ds_read_b128 v[116:119], v94 offset:8192
	v_mul_f32_e32 v77, 0x3c010204, v77
	v_mul_f32_e32 v84, 0x3c010204, v84
	v_mfma_f32_16x16x32_bf16 v[194:197], v[128:131], v[8:11], v[194:197]
	v_lshrrev_b32_e32 v79, 23, v77
	v_lshrrev_b32_e32 v110, 23, v84
	v_mfma_f32_16x16x32_bf16 v[198:201], v[132:135], v[8:11], v[198:201]
	v_and_b32_e32 v77, 0x7f800000, v77
	v_and_b32_e32 v84, 0x7f800000, v84
	v_mfma_f32_16x16x32_bf16 v[202:205], v[128:131], v[40:43], v[202:205]
	v_sub_u32_e32 v77, 0x7e800000, v77
	v_sub_u32_e32 v84, 0x7e800000, v84
	v_mfma_f32_16x16x32_bf16 v[206:209], v[132:135], v[40:43], v[206:209]
	ds_read_b128 v[120:123], v95
	ds_read_b128 v[124:127], v95 offset:8192
	v_fmaak_f32 v78, v178, v77, 0x43000000
	v_fmaak_f32 v85, v186, v84, 0x43000000
	v_mfma_f32_16x16x32_bf16 v[194:197], v[136:139], v[12:15], v[194:197]
	v_cvt_pk_u8_f32 v80, v78, 0, 0
	v_cvt_pk_u8_f32 v82, v85, 0, 0
	v_mfma_f32_16x16x32_bf16 v[198:201], v[140:143], v[12:15], v[198:201]
	v_fmaak_f32 v78, v179, v77, 0x43000000
	v_fmaak_f32 v85, v187, v84, 0x43000000
	v_mfma_f32_16x16x32_bf16 v[202:205], v[136:139], v[44:47], v[202:205]
	v_cvt_pk_u8_f32 v80, v78, 1, v80
	v_cvt_pk_u8_f32 v82, v85, 1, v82
	v_mfma_f32_16x16x32_bf16 v[206:209], v[140:143], v[44:47], v[206:209]
	ds_read_b128 v[128:131], v96
	ds_read_b128 v[132:135], v96 offset:8192
	v_fmaak_f32 v78, v180, v77, 0x43000000
	v_fmaak_f32 v85, v188, v84, 0x43000000
	v_mfma_f32_16x16x32_bf16 v[194:197], v[144:147], v[16:19], v[194:197]
	v_cvt_pk_u8_f32 v80, v78, 2, v80
	v_cvt_pk_u8_f32 v82, v85, 2, v82
	v_mfma_f32_16x16x32_bf16 v[198:201], v[148:151], v[16:19], v[198:201]
	v_fmaak_f32 v78, v181, v77, 0x43000000
	v_fmaak_f32 v85, v189, v84, 0x43000000
	v_mfma_f32_16x16x32_bf16 v[202:205], v[144:147], v[48:51], v[202:205]
	v_cvt_pk_u8_f32 v80, v78, 3, v80
	v_cvt_pk_u8_f32 v82, v85, 3, v82
	v_mfma_f32_16x16x32_bf16 v[206:209], v[148:151], v[48:51], v[206:209]
	ds_read_b128 v[136:139], v97
	ds_read_b128 v[140:143], v97 offset:8192
	v_fmaak_f32 v78, v182, v77, 0x43000000
	v_fmaak_f32 v85, v190, v84, 0x43000000
	v_mfma_f32_16x16x32_bf16 v[194:197], v[152:155], v[20:23], v[194:197]
	v_cvt_pk_u8_f32 v81, v78, 0, 0
	v_cvt_pk_u8_f32 v83, v85, 0, 0
	v_mfma_f32_16x16x32_bf16 v[198:201], v[156:159], v[20:23], v[198:201]
	v_fmaak_f32 v78, v183, v77, 0x43000000
	v_fmaak_f32 v85, v191, v84, 0x43000000
	v_mfma_f32_16x16x32_bf16 v[202:205], v[152:155], v[52:55], v[202:205]
	v_cvt_pk_u8_f32 v81, v78, 1, v81
	v_cvt_pk_u8_f32 v83, v85, 1, v83
	v_mfma_f32_16x16x32_bf16 v[206:209], v[156:159], v[52:55], v[206:209]
	ds_read_b128 v[144:147], v98
	ds_read_b128 v[148:151], v98 offset:8192
	v_fmaak_f32 v78, v184, v77, 0x43000000
	v_fmaak_f32 v85, v192, v84, 0x43000000
	v_mfma_f32_16x16x32_bf16 v[194:197], v[160:163], v[24:27], v[194:197]
	v_cvt_pk_u8_f32 v81, v78, 2, v81
	v_cvt_pk_u8_f32 v83, v85, 2, v83
	v_mfma_f32_16x16x32_bf16 v[198:201], v[164:167], v[24:27], v[198:201]
	v_fmaak_f32 v78, v185, v77, 0x43000000
	v_fmaak_f32 v85, v193, v84, 0x43000000
	v_mfma_f32_16x16x32_bf16 v[202:205], v[160:163], v[56:59], v[202:205]
	v_cvt_pk_u8_f32 v81, v78, 3, v81
	v_cvt_pk_u8_f32 v83, v85, 3, v83
	v_mfma_f32_16x16x32_bf16 v[206:209], v[164:167], v[56:59], v[206:209]
	ds_read_b128 v[152:155], v99
	ds_read_b128 v[156:159], v99 offset:8192
	v_add_u16_e32 v79, 1, v79
	v_add_u16_e32 v110, 1, v110
	v_mfma_f32_16x16x32_bf16 v[194:197], v[168:171], v[28:31], v[194:197]
	ds_write_b8 v106, v79 offset:136
	ds_write_b8 v106, v110 offset:2696
	v_mfma_f32_16x16x32_bf16 v[198:201], v[172:175], v[28:31], v[198:201]
	ds_write2st64_b64 v108, v[80:81], v[82:83] offset1:5
	v_mfma_f32_16x16x32_bf16 v[202:205], v[168:171], v[60:63], v[202:205]
	v_mfma_f32_16x16x32_bf16 v[206:209], v[172:175], v[60:63], v[206:209]
	s_mov_b32 s36, 6
.Ldown_mid:
	s_waitcnt vmcnt(2) lgkmcnt(0)
	s_barrier
	s_add_i32 m0, s30, 0xc000
	s_nop 0
	global_load_lds_dwordx4 v176, s[16:17]
	s_add_i32 m0, s30, 0xe000
	s_nop 0
	global_load_lds_dwordx4 v64, s[16:17]
	s_add_u32 s16, s16, 0x4000
	s_addc_u32 s17, s17, 0
	v_mfma_f32_16x16x32_bf16 v[178:181], v[112:115], v[0:3], 0
	v_mfma_f32_16x16x32_bf16 v[182:185], v[116:119], v[0:3], 0
	ds_read_b128 v[160:163], v100 offset:16384
	ds_read_b128 v[164:167], v100 offset:24576
	v_mfma_f32_16x16x32_bf16 v[186:189], v[112:115], v[32:35], 0
	v_mfma_f32_16x16x32_bf16 v[190:193], v[116:119], v[32:35], 0
	ds_read_b128 v[168:171], v101 offset:16384
	ds_read_b128 v[172:175], v101 offset:24576
	v_max3_f32 v77, |v194|, |v195|, |v196|
	v_max3_f32 v84, |v202|, |v203|, |v204|
	v_mfma_f32_16x16x32_bf16 v[178:181], v[120:123], v[4:7], v[178:181]
	v_max3_f32 v78, |v197|, |v198|, |v199|
	v_max3_f32 v85, |v205|, |v206|, |v207|
	v_mfma_f32_16x16x32_bf16 v[182:185], v[124:127], v[4:7], v[182:185]
	v_max3_f32 v77, |v200|, |v201|, v77
	v_max3_f32 v84, |v208|, |v209|, v84
	v_mfma_f32_16x16x32_bf16 v[186:189], v[120:123], v[36:39], v[186:189]
	v_max_f32_e32 v77, v77, v78
	v_max_f32_e32 v84, v84, v85
	v_mfma_f32_16x16x32_bf16 v[190:193], v[124:127], v[36:39], v[190:193]
	ds_read_b128 v[112:115], v94 offset:16384
	ds_read_b128 v[116:119], v94 offset:24576
	v_mul_f32_e32 v77, 0x3c010204, v77
	v_mul_f32_e32 v84, 0x3c010204, v84
	v_mfma_f32_16x16x32_bf16 v[178:181], v[128:131], v[8:11], v[178:181]
	v_lshrrev_b32_e32 v79, 23, v77
	v_lshrrev_b32_e32 v110, 23, v84
	v_mfma_f32_16x16x32_bf16 v[182:185], v[132:135], v[8:11], v[182:185]
	v_and_b32_e32 v77, 0x7f800000, v77
	v_and_b32_e32 v84, 0x7f800000, v84
	v_mfma_f32_16x16x32_bf16 v[186:189], v[128:131], v[40:43], v[186:189]
	v_sub_u32_e32 v77, 0x7e800000, v77
	v_sub_u32_e32 v84, 0x7e800000, v84
	v_mfma_f32_16x16x32_bf16 v[190:193], v[132:135], v[40:43], v[190:193]
	ds_read_b128 v[120:123], v95 offset:16384
	ds_read_b128 v[124:127], v95 offset:24576
	v_fmaak_f32 v78, v194, v77, 0x43000000
	v_fmaak_f32 v85, v202, v84, 0x43000000
	v_mfma_f32_16x16x32_bf16 v[178:181], v[136:139], v[12:15], v[178:181]
	v_cvt_pk_u8_f32 v80, v78, 0, 0
	v_cvt_pk_u8_f32 v82, v85, 0, 0
	v_mfma_f32_16x16x32_bf16 v[182:185], v[140:143], v[12:15], v[182:185]
	v_fmaak_f32 v78, v195, v77, 0x43000000
	v_fmaak_f32 v85, v203, v84, 0x43000000
	v_mfma_f32_16x16x32_bf16 v[186:189], v[136:139], v[44:47], v[186:189]
	v_cvt_pk_u8_f32 v80, v78, 1, v80
	v_cvt_pk_u8_f32 v82, v85, 1, v82
	v_mfma_f32_16x16x32_bf16 v[190:193], v[140:143], v[44:47], v[190:193]
	ds_read_b128 v[128:131], v96 offset:16384
	ds_read_b128 v[132:135], v96 offset:24576
	v_fmaak_f32 v78, v196, v77, 0x43000000
	v_fmaak_f32 v85, v204, v84, 0x43000000
	v_mfma_f32_16x16x32_bf16 v[178:181], v[144:147], v[16:19], v[178:181]
	v_cvt_pk_u8_f32 v80, v78, 2, v80
	v_cvt_pk_u8_f32 v82, v85, 2, v82
	v_mfma_f32_16x16x32_bf16 v[182:185], v[148:151], v[16:19], v[182:185]
	v_fmaak_f32 v78, v197, v77, 0x43000000
	v_fmaak_f32 v85, v205, v84, 0x43000000
	v_mfma_f32_16x16x32_bf16 v[186:189], v[144:147], v[48:51], v[186:189]
	v_cvt_pk_u8_f32 v80, v78, 3, v80
	v_cvt_pk_u8_f32 v82, v85, 3, v82
	v_mfma_f32_16x16x32_bf16 v[190:193], v[148:151], v[48:51], v[190:193]
	ds_read_b128 v[136:139], v97 offset:16384
	ds_read_b128 v[140:143], v97 offset:24576
	v_fmaak_f32 v78, v198, v77, 0x43000000
	v_fmaak_f32 v85, v206, v84, 0x43000000
	v_mfma_f32_16x16x32_bf16 v[178:181], v[152:155], v[20:23], v[178:181]
	v_cvt_pk_u8_f32 v81, v78, 0, 0
	v_cvt_pk_u8_f32 v83, v85, 0, 0
	v_mfma_f32_16x16x32_bf16 v[182:185], v[156:159], v[20:23], v[182:185]
	v_fmaak_f32 v78, v199, v77, 0x43000000
	v_fmaak_f32 v85, v207, v84, 0x43000000
	v_mfma_f32_16x16x32_bf16 v[186:189], v[152:155], v[52:55], v[186:189]
	v_cvt_pk_u8_f32 v81, v78, 1, v81
	v_cvt_pk_u8_f32 v83, v85, 1, v83
	v_mfma_f32_16x16x32_bf16 v[190:193], v[156:159], v[52:55], v[190:193]
	ds_read_b128 v[144:147], v98 offset:16384
	ds_read_b128 v[148:151], v98 offset:24576
	v_fmaak_f32 v78, v200, v77, 0x43000000
	v_fmaak_f32 v85, v208, v84, 0x43000000
	v_mfma_f32_16x16x32_bf16 v[178:181], v[210:213], v[24:27], v[178:181]
	v_cvt_pk_u8_f32 v81, v78, 2, v81
	v_cvt_pk_u8_f32 v83, v85, 2, v83
	v_mfma_f32_16x16x32_bf16 v[182:185], v[214:217], v[24:27], v[182:185]
	v_fmaak_f32 v78, v201, v77, 0x43000000
	v_fmaak_f32 v85, v209, v84, 0x43000000
	v_mfma_f32_16x16x32_bf16 v[186:189], v[210:213], v[56:59], v[186:189]
	v_cvt_pk_u8_f32 v81, v78, 3, v81
	v_cvt_pk_u8_f32 v83, v85, 3, v83
	v_mfma_f32_16x16x32_bf16 v[190:193], v[214:217], v[56:59], v[190:193]
	ds_read_b128 v[152:155], v99 offset:16384
	ds_read_b128 v[156:159], v99 offset:24576
	v_add_u16_e32 v79, 1, v79
	v_add_u16_e32 v110, 1, v110
	v_mfma_f32_16x16x32_bf16 v[178:181], v[236:239], v[28:31], v[178:181]
	ds_write_b8 v106, v79 offset:140
	ds_write_b8 v106, v110 offset:2700
	v_mfma_f32_16x16x32_bf16 v[182:185], v[240:243], v[28:31], v[182:185]
	ds_write2st64_b64 v109, v[80:81], v[82:83] offset1:5
	v_mfma_f32_16x16x32_bf16 v[186:189], v[236:239], v[60:63], v[186:189]
	v_mfma_f32_16x16x32_bf16 v[190:193], v[240:243], v[60:63], v[190:193]
	s_waitcnt lgkmcnt(0)
	ds_read_b128 v[194:197], v103
	ds_read_b128 v[198:201], v103 offset:1280
	ds_read_b128 v[202:205], v103 offset:2560
	ds_read_b128 v[206:209], v103 offset:3840
	ds_read_b128 v[244:247], v104 offset:128
	s_waitcnt vmcnt(2) lgkmcnt(0)
	s_barrier
	global_store_dwordx4 v72, v[194:197], s[10:11]
	global_store_dwordx4 v73, v[198:201], s[10:11]
	global_store_dwordx4 v74, v[202:205], s[10:11]
	global_store_dwordx4 v75, v[206:209], s[10:11]
	s_and_saveexec_b64 s[8:9], s[2:3]
	global_store_dwordx4 v76, v[244:247], s[10:11]
	s_or_b64 exec, exec, s[8:9]
	v_add_u32_e32 v72, 0x80, v72
	v_add_u32_e32 v73, 0x80, v73
	v_add_u32_e32 v74, 0x80, v74
	v_add_u32_e32 v75, 0x80, v75
	v_add_u32_e32 v76, 16, v76
	s_mov_b32 m0, s30
	s_nop 0
	global_load_lds_dwordx4 v176, s[16:17]
	s_add_i32 m0, s30, 0x2000
	s_nop 0
	global_load_lds_dwordx4 v64, s[16:17]
	s_add_u32 s16, s16, 0x4000
	s_addc_u32 s17, s17, 0
	v_mfma_f32_16x16x32_bf16 v[194:197], v[112:115], v[0:3], 0
	v_mfma_f32_16x16x32_bf16 v[198:201], v[116:119], v[0:3], 0
	ds_read_b128 v[210:213], v100 offset:32768
	ds_read_b128 v[214:217], v100 offset:40960
	v_mfma_f32_16x16x32_bf16 v[202:205], v[112:115], v[32:35], 0
	v_mfma_f32_16x16x32_bf16 v[206:209], v[116:119], v[32:35], 0
	ds_read_b128 v[236:239], v101 offset:32768
	ds_read_b128 v[240:243], v101 offset:40960
	v_max3_f32 v77, |v178|, |v179|, |v180|
	v_max3_f32 v84, |v186|, |v187|, |v188|
	v_mfma_f32_16x16x32_bf16 v[194:197], v[120:123], v[4:7], v[194:197]
	v_max3_f32 v78, |v181|, |v182|, |v183|
	v_max3_f32 v85, |v189|, |v190|, |v191|
	v_mfma_f32_16x16x32_bf16 v[198:201], v[124:127], v[4:7], v[198:201]
	v_max3_f32 v77, |v184|, |v185|, v77
	v_max3_f32 v84, |v192|, |v193|, v84
	v_mfma_f32_16x16x32_bf16 v[202:205], v[120:123], v[36:39], v[202:205]
	v_max_f32_e32 v77, v77, v78
	v_max_f32_e32 v84, v84, v85
	v_mfma_f32_16x16x32_bf16 v[206:209], v[124:127], v[36:39], v[206:209]
	ds_read_b128 v[112:115], v94 offset:32768
	ds_read_b128 v[116:119], v94 offset:40960
	v_mul_f32_e32 v77, 0x3c010204, v77
	v_mul_f32_e32 v84, 0x3c010204, v84
	v_mfma_f32_16x16x32_bf16 v[194:197], v[128:131], v[8:11], v[194:197]
	v_lshrrev_b32_e32 v79, 23, v77
	v_lshrrev_b32_e32 v110, 23, v84
	v_mfma_f32_16x16x32_bf16 v[198:201], v[132:135], v[8:11], v[198:201]
	v_and_b32_e32 v77, 0x7f800000, v77
	v_and_b32_e32 v84, 0x7f800000, v84
	v_mfma_f32_16x16x32_bf16 v[202:205], v[128:131], v[40:43], v[202:205]
	v_sub_u32_e32 v77, 0x7e800000, v77
	v_sub_u32_e32 v84, 0x7e800000, v84
	v_mfma_f32_16x16x32_bf16 v[206:209], v[132:135], v[40:43], v[206:209]
	ds_read_b128 v[120:123], v95 offset:32768
	ds_read_b128 v[124:127], v95 offset:40960
	v_fmaak_f32 v78, v178, v77, 0x43000000
	v_fmaak_f32 v85, v186, v84, 0x43000000
	v_mfma_f32_16x16x32_bf16 v[194:197], v[136:139], v[12:15], v[194:197]
	v_cvt_pk_u8_f32 v80, v78, 0, 0
	v_cvt_pk_u8_f32 v82, v85, 0, 0
	v_mfma_f32_16x16x32_bf16 v[198:201], v[140:143], v[12:15], v[198:201]
	v_fmaak_f32 v78, v179, v77, 0x43000000
	v_fmaak_f32 v85, v187, v84, 0x43000000
	v_mfma_f32_16x16x32_bf16 v[202:205], v[136:139], v[44:47], v[202:205]
	v_cvt_pk_u8_f32 v80, v78, 1, v80
	v_cvt_pk_u8_f32 v82, v85, 1, v82
	v_mfma_f32_16x16x32_bf16 v[206:209], v[140:143], v[44:47], v[206:209]
	ds_read_b128 v[128:131], v96 offset:32768
	ds_read_b128 v[132:135], v96 offset:40960
	v_fmaak_f32 v78, v180, v77, 0x43000000
	v_fmaak_f32 v85, v188, v84, 0x43000000
	v_mfma_f32_16x16x32_bf16 v[194:197], v[144:147], v[16:19], v[194:197]
	v_cvt_pk_u8_f32 v80, v78, 2, v80
	v_cvt_pk_u8_f32 v82, v85, 2, v82
	v_mfma_f32_16x16x32_bf16 v[198:201], v[148:151], v[16:19], v[198:201]
	v_fmaak_f32 v78, v181, v77, 0x43000000
	v_fmaak_f32 v85, v189, v84, 0x43000000
	v_mfma_f32_16x16x32_bf16 v[202:205], v[144:147], v[48:51], v[202:205]
	v_cvt_pk_u8_f32 v80, v78, 3, v80
	v_cvt_pk_u8_f32 v82, v85, 3, v82
	v_mfma_f32_16x16x32_bf16 v[206:209], v[148:151], v[48:51], v[206:209]
	ds_read_b128 v[136:139], v97 offset:32768
	ds_read_b128 v[140:143], v97 offset:40960
	v_fmaak_f32 v78, v182, v77, 0x43000000
	v_fmaak_f32 v85, v190, v84, 0x43000000
	v_mfma_f32_16x16x32_bf16 v[194:197], v[152:155], v[20:23], v[194:197]
	v_cvt_pk_u8_f32 v81, v78, 0, 0
	v_cvt_pk_u8_f32 v83, v85, 0, 0
	v_mfma_f32_16x16x32_bf16 v[198:201], v[156:159], v[20:23], v[198:201]
	v_fmaak_f32 v78, v183, v77, 0x43000000
	v_fmaak_f32 v85, v191, v84, 0x43000000
	v_mfma_f32_16x16x32_bf16 v[202:205], v[152:155], v[52:55], v[202:205]
	v_cvt_pk_u8_f32 v81, v78, 1, v81
	v_cvt_pk_u8_f32 v83, v85, 1, v83
	v_mfma_f32_16x16x32_bf16 v[206:209], v[156:159], v[52:55], v[206:209]
	ds_read_b128 v[144:147], v98 offset:32768
	ds_read_b128 v[148:151], v98 offset:40960
	v_fmaak_f32 v78, v184, v77, 0x43000000
	v_fmaak_f32 v85, v192, v84, 0x43000000
	v_mfma_f32_16x16x32_bf16 v[194:197], v[160:163], v[24:27], v[194:197]
	v_cvt_pk_u8_f32 v81, v78, 2, v81
	v_cvt_pk_u8_f32 v83, v85, 2, v83
	v_mfma_f32_16x16x32_bf16 v[198:201], v[164:167], v[24:27], v[198:201]
	v_fmaak_f32 v78, v185, v77, 0x43000000
	v_fmaak_f32 v85, v193, v84, 0x43000000
	v_mfma_f32_16x16x32_bf16 v[202:205], v[160:163], v[56:59], v[202:205]
	v_cvt_pk_u8_f32 v81, v78, 3, v81
	v_cvt_pk_u8_f32 v83, v85, 3, v83
	v_mfma_f32_16x16x32_bf16 v[206:209], v[164:167], v[56:59], v[206:209]
	ds_read_b128 v[152:155], v99 offset:32768
	ds_read_b128 v[156:159], v99 offset:40960
	v_add_u16_e32 v79, 1, v79
	v_add_u16_e32 v110, 1, v110
	v_mfma_f32_16x16x32_bf16 v[194:197], v[168:171], v[28:31], v[194:197]
	ds_write_b8 v106, v79 offset:128
	ds_write_b8 v106, v110 offset:2688
	v_mfma_f32_16x16x32_bf16 v[198:201], v[172:175], v[28:31], v[198:201]
	ds_write2st64_b64 v102, v[80:81], v[82:83] offset1:5
	v_mfma_f32_16x16x32_bf16 v[202:205], v[168:171], v[60:63], v[202:205]
	v_mfma_f32_16x16x32_bf16 v[206:209], v[172:175], v[60:63], v[206:209]
	s_waitcnt vmcnt(7) lgkmcnt(0)
	s_barrier
	s_add_i32 m0, s30, 0x4000
	s_nop 0
	global_load_lds_dwordx4 v176, s[16:17]
	s_add_i32 m0, s30, 0x6000
	s_nop 0
	global_load_lds_dwordx4 v64, s[16:17]
	s_add_u32 s16, s16, 0x4000
	s_addc_u32 s17, s17, 0
	v_mfma_f32_16x16x32_bf16 v[178:181], v[112:115], v[0:3], 0
	v_mfma_f32_16x16x32_bf16 v[182:185], v[116:119], v[0:3], 0
	ds_read_b128 v[160:163], v100 offset:49152
	ds_read_b128 v[164:167], v100 offset:57344
	v_mfma_f32_16x16x32_bf16 v[186:189], v[112:115], v[32:35], 0
	v_mfma_f32_16x16x32_bf16 v[190:193], v[116:119], v[32:35], 0
	ds_read_b128 v[168:171], v101 offset:49152
	ds_read_b128 v[172:175], v101 offset:57344
	v_max3_f32 v77, |v194|, |v195|, |v196|
	v_max3_f32 v84, |v202|, |v203|, |v204|
	v_mfma_f32_16x16x32_bf16 v[178:181], v[120:123], v[4:7], v[178:181]
	v_max3_f32 v78, |v197|, |v198|, |v199|
	v_max3_f32 v85, |v205|, |v206|, |v207|
	v_mfma_f32_16x16x32_bf16 v[182:185], v[124:127], v[4:7], v[182:185]
	v_max3_f32 v77, |v200|, |v201|, v77
	v_max3_f32 v84, |v208|, |v209|, v84
	v_mfma_f32_16x16x32_bf16 v[186:189], v[120:123], v[36:39], v[186:189]
	v_max_f32_e32 v77, v77, v78
	v_max_f32_e32 v84, v84, v85
	v_mfma_f32_16x16x32_bf16 v[190:193], v[124:127], v[36:39], v[190:193]
	ds_read_b128 v[112:115], v94 offset:49152
	ds_read_b128 v[116:119], v94 offset:57344
	v_mul_f32_e32 v77, 0x3c010204, v77
	v_mul_f32_e32 v84, 0x3c010204, v84
	v_mfma_f32_16x16x32_bf16 v[178:181], v[128:131], v[8:11], v[178:181]
	v_lshrrev_b32_e32 v79, 23, v77
	v_lshrrev_b32_e32 v110, 23, v84
	v_mfma_f32_16x16x32_bf16 v[182:185], v[132:135], v[8:11], v[182:185]
	v_and_b32_e32 v77, 0x7f800000, v77
	v_and_b32_e32 v84, 0x7f800000, v84
	v_mfma_f32_16x16x32_bf16 v[186:189], v[128:131], v[40:43], v[186:189]
	v_sub_u32_e32 v77, 0x7e800000, v77
	v_sub_u32_e32 v84, 0x7e800000, v84
	v_mfma_f32_16x16x32_bf16 v[190:193], v[132:135], v[40:43], v[190:193]
	ds_read_b128 v[120:123], v95 offset:49152
	ds_read_b128 v[124:127], v95 offset:57344
	v_fmaak_f32 v78, v194, v77, 0x43000000
	v_fmaak_f32 v85, v202, v84, 0x43000000
	v_mfma_f32_16x16x32_bf16 v[178:181], v[136:139], v[12:15], v[178:181]
	v_cvt_pk_u8_f32 v80, v78, 0, 0
	v_cvt_pk_u8_f32 v82, v85, 0, 0
	v_mfma_f32_16x16x32_bf16 v[182:185], v[140:143], v[12:15], v[182:185]
	v_fmaak_f32 v78, v195, v77, 0x43000000
	v_fmaak_f32 v85, v203, v84, 0x43000000
	v_mfma_f32_16x16x32_bf16 v[186:189], v[136:139], v[44:47], v[186:189]
	v_cvt_pk_u8_f32 v80, v78, 1, v80
	v_cvt_pk_u8_f32 v82, v85, 1, v82
	v_mfma_f32_16x16x32_bf16 v[190:193], v[140:143], v[44:47], v[190:193]
	ds_read_b128 v[128:131], v96 offset:49152
	ds_read_b128 v[132:135], v96 offset:57344
	v_fmaak_f32 v78, v196, v77, 0x43000000
	v_fmaak_f32 v85, v204, v84, 0x43000000
	v_mfma_f32_16x16x32_bf16 v[178:181], v[144:147], v[16:19], v[178:181]
	v_cvt_pk_u8_f32 v80, v78, 2, v80
	v_cvt_pk_u8_f32 v82, v85, 2, v82
	v_mfma_f32_16x16x32_bf16 v[182:185], v[148:151], v[16:19], v[182:185]
	v_fmaak_f32 v78, v197, v77, 0x43000000
	v_fmaak_f32 v85, v205, v84, 0x43000000
	v_mfma_f32_16x16x32_bf16 v[186:189], v[144:147], v[48:51], v[186:189]
	v_cvt_pk_u8_f32 v80, v78, 3, v80
	v_cvt_pk_u8_f32 v82, v85, 3, v82
	v_mfma_f32_16x16x32_bf16 v[190:193], v[148:151], v[48:51], v[190:193]
	ds_read_b128 v[136:139], v97 offset:49152
	ds_read_b128 v[140:143], v97 offset:57344
	v_fmaak_f32 v78, v198, v77, 0x43000000
	v_fmaak_f32 v85, v206, v84, 0x43000000
	v_mfma_f32_16x16x32_bf16 v[178:181], v[152:155], v[20:23], v[178:181]
	v_cvt_pk_u8_f32 v81, v78, 0, 0
	v_cvt_pk_u8_f32 v83, v85, 0, 0
	v_mfma_f32_16x16x32_bf16 v[182:185], v[156:159], v[20:23], v[182:185]
	v_fmaak_f32 v78, v199, v77, 0x43000000
	v_fmaak_f32 v85, v207, v84, 0x43000000
	v_mfma_f32_16x16x32_bf16 v[186:189], v[152:155], v[52:55], v[186:189]
	v_cvt_pk_u8_f32 v81, v78, 1, v81
	v_cvt_pk_u8_f32 v83, v85, 1, v83
	v_mfma_f32_16x16x32_bf16 v[190:193], v[156:159], v[52:55], v[190:193]
	ds_read_b128 v[144:147], v98 offset:49152
	ds_read_b128 v[148:151], v98 offset:57344
	v_fmaak_f32 v78, v200, v77, 0x43000000
	v_fmaak_f32 v85, v208, v84, 0x43000000
	v_mfma_f32_16x16x32_bf16 v[178:181], v[210:213], v[24:27], v[178:181]
	v_cvt_pk_u8_f32 v81, v78, 2, v81
	v_cvt_pk_u8_f32 v83, v85, 2, v83
	v_mfma_f32_16x16x32_bf16 v[182:185], v[214:217], v[24:27], v[182:185]
	v_fmaak_f32 v78, v201, v77, 0x43000000
	v_fmaak_f32 v85, v209, v84, 0x43000000
	v_mfma_f32_16x16x32_bf16 v[186:189], v[210:213], v[56:59], v[186:189]
	v_cvt_pk_u8_f32 v81, v78, 3, v81
	v_cvt_pk_u8_f32 v83, v85, 3, v83
	v_mfma_f32_16x16x32_bf16 v[190:193], v[214:217], v[56:59], v[190:193]
	ds_read_b128 v[152:155], v99 offset:49152
	ds_read_b128 v[156:159], v99 offset:57344
	v_add_u16_e32 v79, 1, v79
	v_add_u16_e32 v110, 1, v110
	v_mfma_f32_16x16x32_bf16 v[178:181], v[236:239], v[28:31], v[178:181]
	ds_write_b8 v106, v79 offset:132
	ds_write_b8 v106, v110 offset:2692
	v_mfma_f32_16x16x32_bf16 v[182:185], v[240:243], v[28:31], v[182:185]
	ds_write2st64_b64 v107, v[80:81], v[82:83] offset1:5
	v_mfma_f32_16x16x32_bf16 v[186:189], v[236:239], v[60:63], v[186:189]
	v_mfma_f32_16x16x32_bf16 v[190:193], v[240:243], v[60:63], v[190:193]
	s_waitcnt vmcnt(2) lgkmcnt(0)
	s_barrier
	s_add_i32 m0, s30, 0x8000
	s_nop 0
	global_load_lds_dwordx4 v176, s[16:17]
	s_add_i32 m0, s30, 0xa000
	s_nop 0
	global_load_lds_dwordx4 v64, s[16:17]
	s_add_u32 s16, s16, 0x4000
	s_addc_u32 s17, s17, 0
	v_mfma_f32_16x16x32_bf16 v[194:197], v[112:115], v[0:3], 0
	v_mfma_f32_16x16x32_bf16 v[198:201], v[116:119], v[0:3], 0
	ds_read_b128 v[210:213], v100
	ds_read_b128 v[214:217], v100 offset:8192
	v_mfma_f32_16x16x32_bf16 v[202:205], v[112:115], v[32:35], 0
	v_mfma_f32_16x16x32_bf16 v[206:209], v[116:119], v[32:35], 0
	ds_read_b128 v[236:239], v101
	ds_read_b128 v[240:243], v101 offset:8192
	v_max3_f32 v77, |v178|, |v179|, |v180|
	v_max3_f32 v84, |v186|, |v187|, |v188|
	v_mfma_f32_16x16x32_bf16 v[194:197], v[120:123], v[4:7], v[194:197]
	v_max3_f32 v78, |v181|, |v182|, |v183|
	v_max3_f32 v85, |v189|, |v190|, |v191|
	v_mfma_f32_16x16x32_bf16 v[198:201], v[124:127], v[4:7], v[198:201]
	v_max3_f32 v77, |v184|, |v185|, v77
	v_max3_f32 v84, |v192|, |v193|, v84
	v_mfma_f32_16x16x32_bf16 v[202:205], v[120:123], v[36:39], v[202:205]
	v_max_f32_e32 v77, v77, v78
	v_max_f32_e32 v84, v84, v85
	v_mfma_f32_16x16x32_bf16 v[206:209], v[124:127], v[36:39], v[206:209]
	ds_read_b128 v[112:115], v94
	ds_read_b128 v[116:119], v94 offset:8192
	v_mul_f32_e32 v77, 0x3c010204, v77
	v_mul_f32_e32 v84, 0x3c010204, v84
	v_mfma_f32_16x16x32_bf16 v[194:197], v[128:131], v[8:11], v[194:197]
	v_lshrrev_b32_e32 v79, 23, v77
	v_lshrrev_b32_e32 v110, 23, v84
	v_mfma_f32_16x16x32_bf16 v[198:201], v[132:135], v[8:11], v[198:201]
	v_and_b32_e32 v77, 0x7f800000, v77
	v_and_b32_e32 v84, 0x7f800000, v84
	v_mfma_f32_16x16x32_bf16 v[202:205], v[128:131], v[40:43], v[202:205]
	v_sub_u32_e32 v77, 0x7e800000, v77
	v_sub_u32_e32 v84, 0x7e800000, v84
	v_mfma_f32_16x16x32_bf16 v[206:209], v[132:135], v[40:43], v[206:209]
	ds_read_b128 v[120:123], v95
	ds_read_b128 v[124:127], v95 offset:8192
	v_fmaak_f32 v78, v178, v77, 0x43000000
	v_fmaak_f32 v85, v186, v84, 0x43000000
	v_mfma_f32_16x16x32_bf16 v[194:197], v[136:139], v[12:15], v[194:197]
	v_cvt_pk_u8_f32 v80, v78, 0, 0
	v_cvt_pk_u8_f32 v82, v85, 0, 0
	v_mfma_f32_16x16x32_bf16 v[198:201], v[140:143], v[12:15], v[198:201]
	v_fmaak_f32 v78, v179, v77, 0x43000000
	v_fmaak_f32 v85, v187, v84, 0x43000000
	v_mfma_f32_16x16x32_bf16 v[202:205], v[136:139], v[44:47], v[202:205]
	v_cvt_pk_u8_f32 v80, v78, 1, v80
	v_cvt_pk_u8_f32 v82, v85, 1, v82
	v_mfma_f32_16x16x32_bf16 v[206:209], v[140:143], v[44:47], v[206:209]
	ds_read_b128 v[128:131], v96
	ds_read_b128 v[132:135], v96 offset:8192
	v_fmaak_f32 v78, v180, v77, 0x43000000
	v_fmaak_f32 v85, v188, v84, 0x43000000
	v_mfma_f32_16x16x32_bf16 v[194:197], v[144:147], v[16:19], v[194:197]
	v_cvt_pk_u8_f32 v80, v78, 2, v80
	v_cvt_pk_u8_f32 v82, v85, 2, v82
	v_mfma_f32_16x16x32_bf16 v[198:201], v[148:151], v[16:19], v[198:201]
	v_fmaak_f32 v78, v181, v77, 0x43000000
	v_fmaak_f32 v85, v189, v84, 0x43000000
	v_mfma_f32_16x16x32_bf16 v[202:205], v[144:147], v[48:51], v[202:205]
	v_cvt_pk_u8_f32 v80, v78, 3, v80
	v_cvt_pk_u8_f32 v82, v85, 3, v82
	v_mfma_f32_16x16x32_bf16 v[206:209], v[148:151], v[48:51], v[206:209]
	ds_read_b128 v[136:139], v97
	ds_read_b128 v[140:143], v97 offset:8192
	v_fmaak_f32 v78, v182, v77, 0x43000000
	v_fmaak_f32 v85, v190, v84, 0x43000000
	v_mfma_f32_16x16x32_bf16 v[194:197], v[152:155], v[20:23], v[194:197]
	v_cvt_pk_u8_f32 v81, v78, 0, 0
	v_cvt_pk_u8_f32 v83, v85, 0, 0
	v_mfma_f32_16x16x32_bf16 v[198:201], v[156:159], v[20:23], v[198:201]
	v_fmaak_f32 v78, v183, v77, 0x43000000
	v_fmaak_f32 v85, v191, v84, 0x43000000
	v_mfma_f32_16x16x32_bf16 v[202:205], v[152:155], v[52:55], v[202:205]
	v_cvt_pk_u8_f32 v81, v78, 1, v81
	v_cvt_pk_u8_f32 v83, v85, 1, v83
	v_mfma_f32_16x16x32_bf16 v[206:209], v[156:159], v[52:55], v[206:209]
	ds_read_b128 v[144:147], v98
	ds_read_b128 v[148:151], v98 offset:8192
	v_fmaak_f32 v78, v184, v77, 0x43000000
	v_fmaak_f32 v85, v192, v84, 0x43000000
	v_mfma_f32_16x16x32_bf16 v[194:197], v[160:163], v[24:27], v[194:197]
	v_cvt_pk_u8_f32 v81, v78, 2, v81
	v_cvt_pk_u8_f32 v83, v85, 2, v83
	v_mfma_f32_16x16x32_bf16 v[198:201], v[164:167], v[24:27], v[198:201]
	v_fmaak_f32 v78, v185, v77, 0x43000000
	v_fmaak_f32 v85, v193, v84, 0x43000000
	v_mfma_f32_16x16x32_bf16 v[202:205], v[160:163], v[56:59], v[202:205]
	v_cvt_pk_u8_f32 v81, v78, 3, v81
	v_cvt_pk_u8_f32 v83, v85, 3, v83
	v_mfma_f32_16x16x32_bf16 v[206:209], v[164:167], v[56:59], v[206:209]
	ds_read_b128 v[152:155], v99
	ds_read_b128 v[156:159], v99 offset:8192
	v_add_u16_e32 v79, 1, v79
	v_add_u16_e32 v110, 1, v110
	v_mfma_f32_16x16x32_bf16 v[194:197], v[168:171], v[28:31], v[194:197]
	ds_write_b8 v106, v79 offset:136
	ds_write_b8 v106, v110 offset:2696
	v_mfma_f32_16x16x32_bf16 v[198:201], v[172:175], v[28:31], v[198:201]
	ds_write2st64_b64 v108, v[80:81], v[82:83] offset1:5
	v_mfma_f32_16x16x32_bf16 v[202:205], v[168:171], v[60:63], v[202:205]
	v_mfma_f32_16x16x32_bf16 v[206:209], v[172:175], v[60:63], v[206:209]
	s_sub_i32 s36, s36, 1
	s_cmp_lg_u32 s36, 0
	s_cbranch_scc1 .Ldown_mid
	s_waitcnt vmcnt(2) lgkmcnt(0)
	s_barrier
	s_add_i32 m0, s30, 0xc000
	s_nop 0
	global_load_lds_dwordx4 v176, s[16:17]
	s_add_i32 m0, s30, 0xe000
	s_nop 0
	global_load_lds_dwordx4 v64, s[16:17]
	s_add_u32 s16, s16, 0x4000
	s_addc_u32 s17, s17, 0
	v_mfma_f32_16x16x32_bf16 v[178:181], v[112:115], v[0:3], 0
	v_mfma_f32_16x16x32_bf16 v[182:185], v[116:119], v[0:3], 0
	ds_read_b128 v[160:163], v100 offset:16384
	ds_read_b128 v[164:167], v100 offset:24576
	v_mfma_f32_16x16x32_bf16 v[186:189], v[112:115], v[32:35], 0
	v_mfma_f32_16x16x32_bf16 v[190:193], v[116:119], v[32:35], 0
	ds_read_b128 v[168:171], v101 offset:16384
	ds_read_b128 v[172:175], v101 offset:24576
	v_max3_f32 v77, |v194|, |v195|, |v196|
	v_max3_f32 v84, |v202|, |v203|, |v204|
	v_mfma_f32_16x16x32_bf16 v[178:181], v[120:123], v[4:7], v[178:181]
	v_max3_f32 v78, |v197|, |v198|, |v199|
	v_max3_f32 v85, |v205|, |v206|, |v207|
	v_mfma_f32_16x16x32_bf16 v[182:185], v[124:127], v[4:7], v[182:185]
	v_max3_f32 v77, |v200|, |v201|, v77
	v_max3_f32 v84, |v208|, |v209|, v84
	v_mfma_f32_16x16x32_bf16 v[186:189], v[120:123], v[36:39], v[186:189]
	v_max_f32_e32 v77, v77, v78
	v_max_f32_e32 v84, v84, v85
	v_mfma_f32_16x16x32_bf16 v[190:193], v[124:127], v[36:39], v[190:193]
	ds_read_b128 v[112:115], v94 offset:16384
	ds_read_b128 v[116:119], v94 offset:24576
	v_mul_f32_e32 v77, 0x3c010204, v77
	v_mul_f32_e32 v84, 0x3c010204, v84
	v_mfma_f32_16x16x32_bf16 v[178:181], v[128:131], v[8:11], v[178:181]
	v_lshrrev_b32_e32 v79, 23, v77
	v_lshrrev_b32_e32 v110, 23, v84
	v_mfma_f32_16x16x32_bf16 v[182:185], v[132:135], v[8:11], v[182:185]
	v_and_b32_e32 v77, 0x7f800000, v77
	v_and_b32_e32 v84, 0x7f800000, v84
	v_mfma_f32_16x16x32_bf16 v[186:189], v[128:131], v[40:43], v[186:189]
	v_sub_u32_e32 v77, 0x7e800000, v77
	v_sub_u32_e32 v84, 0x7e800000, v84
	v_mfma_f32_16x16x32_bf16 v[190:193], v[132:135], v[40:43], v[190:193]
	ds_read_b128 v[120:123], v95 offset:16384
	ds_read_b128 v[124:127], v95 offset:24576
	v_fmaak_f32 v78, v194, v77, 0x43000000
	v_fmaak_f32 v85, v202, v84, 0x43000000
	v_mfma_f32_16x16x32_bf16 v[178:181], v[136:139], v[12:15], v[178:181]
	v_cvt_pk_u8_f32 v80, v78, 0, 0
	v_cvt_pk_u8_f32 v82, v85, 0, 0
	v_mfma_f32_16x16x32_bf16 v[182:185], v[140:143], v[12:15], v[182:185]
	v_fmaak_f32 v78, v195, v77, 0x43000000
	v_fmaak_f32 v85, v203, v84, 0x43000000
	v_mfma_f32_16x16x32_bf16 v[186:189], v[136:139], v[44:47], v[186:189]
	v_cvt_pk_u8_f32 v80, v78, 1, v80
	v_cvt_pk_u8_f32 v82, v85, 1, v82
	v_mfma_f32_16x16x32_bf16 v[190:193], v[140:143], v[44:47], v[190:193]
	ds_read_b128 v[128:131], v96 offset:16384
	ds_read_b128 v[132:135], v96 offset:24576
	v_fmaak_f32 v78, v196, v77, 0x43000000
	v_fmaak_f32 v85, v204, v84, 0x43000000
	v_mfma_f32_16x16x32_bf16 v[178:181], v[144:147], v[16:19], v[178:181]
	v_cvt_pk_u8_f32 v80, v78, 2, v80
	v_cvt_pk_u8_f32 v82, v85, 2, v82
	v_mfma_f32_16x16x32_bf16 v[182:185], v[148:151], v[16:19], v[182:185]
	v_fmaak_f32 v78, v197, v77, 0x43000000
	v_fmaak_f32 v85, v205, v84, 0x43000000
	v_mfma_f32_16x16x32_bf16 v[186:189], v[144:147], v[48:51], v[186:189]
	v_cvt_pk_u8_f32 v80, v78, 3, v80
	v_cvt_pk_u8_f32 v82, v85, 3, v82
	v_mfma_f32_16x16x32_bf16 v[190:193], v[148:151], v[48:51], v[190:193]
	ds_read_b128 v[136:139], v97 offset:16384
	ds_read_b128 v[140:143], v97 offset:24576
	v_fmaak_f32 v78, v198, v77, 0x43000000
	v_fmaak_f32 v85, v206, v84, 0x43000000
	v_mfma_f32_16x16x32_bf16 v[178:181], v[152:155], v[20:23], v[178:181]
	v_cvt_pk_u8_f32 v81, v78, 0, 0
	v_cvt_pk_u8_f32 v83, v85, 0, 0
	v_mfma_f32_16x16x32_bf16 v[182:185], v[156:159], v[20:23], v[182:185]
	v_fmaak_f32 v78, v199, v77, 0x43000000
	v_fmaak_f32 v85, v207, v84, 0x43000000
	v_mfma_f32_16x16x32_bf16 v[186:189], v[152:155], v[52:55], v[186:189]
	v_cvt_pk_u8_f32 v81, v78, 1, v81
	v_cvt_pk_u8_f32 v83, v85, 1, v83
	v_mfma_f32_16x16x32_bf16 v[190:193], v[156:159], v[52:55], v[190:193]
	ds_read_b128 v[144:147], v98 offset:16384
	ds_read_b128 v[148:151], v98 offset:24576
	v_fmaak_f32 v78, v200, v77, 0x43000000
	v_fmaak_f32 v85, v208, v84, 0x43000000
	v_mfma_f32_16x16x32_bf16 v[178:181], v[210:213], v[24:27], v[178:181]
	v_cvt_pk_u8_f32 v81, v78, 2, v81
	v_cvt_pk_u8_f32 v83, v85, 2, v83
	v_mfma_f32_16x16x32_bf16 v[182:185], v[214:217], v[24:27], v[182:185]
	v_fmaak_f32 v78, v201, v77, 0x43000000
	v_fmaak_f32 v85, v209, v84, 0x43000000
	v_mfma_f32_16x16x32_bf16 v[186:189], v[210:213], v[56:59], v[186:189]
	v_cvt_pk_u8_f32 v81, v78, 3, v81
	v_cvt_pk_u8_f32 v83, v85, 3, v83
	v_mfma_f32_16x16x32_bf16 v[190:193], v[214:217], v[56:59], v[190:193]
	ds_read_b128 v[152:155], v99 offset:16384
	ds_read_b128 v[156:159], v99 offset:24576
	v_add_u16_e32 v79, 1, v79
	v_add_u16_e32 v110, 1, v110
	v_mfma_f32_16x16x32_bf16 v[178:181], v[236:239], v[28:31], v[178:181]
	ds_write_b8 v106, v79 offset:140
	ds_write_b8 v106, v110 offset:2700
	v_mfma_f32_16x16x32_bf16 v[182:185], v[240:243], v[28:31], v[182:185]
	ds_write2st64_b64 v109, v[80:81], v[82:83] offset1:5
	v_mfma_f32_16x16x32_bf16 v[186:189], v[236:239], v[60:63], v[186:189]
	v_mfma_f32_16x16x32_bf16 v[190:193], v[240:243], v[60:63], v[190:193]
	s_waitcnt lgkmcnt(0)
	ds_read_b128 v[194:197], v103
	ds_read_b128 v[198:201], v103 offset:1280
	ds_read_b128 v[202:205], v103 offset:2560
	ds_read_b128 v[206:209], v103 offset:3840
	ds_read_b128 v[244:247], v104 offset:128
	s_waitcnt vmcnt(2) lgkmcnt(0)
	s_barrier
	global_store_dwordx4 v72, v[194:197], s[10:11]
	global_store_dwordx4 v73, v[198:201], s[10:11]
	global_store_dwordx4 v74, v[202:205], s[10:11]
	global_store_dwordx4 v75, v[206:209], s[10:11]
	s_and_saveexec_b64 s[8:9], s[2:3]
	global_store_dwordx4 v76, v[244:247], s[10:11]
	s_or_b64 exec, exec, s[8:9]
	v_add_u32_e32 v72, 0x80, v72
	v_add_u32_e32 v73, 0x80, v73
	v_add_u32_e32 v74, 0x80, v74
	v_add_u32_e32 v75, 0x80, v75
	v_add_u32_e32 v76, 16, v76
	v_mfma_f32_16x16x32_bf16 v[194:197], v[112:115], v[0:3], 0
	v_mfma_f32_16x16x32_bf16 v[198:201], v[116:119], v[0:3], 0
	ds_read_b128 v[210:213], v100 offset:32768
	ds_read_b128 v[214:217], v100 offset:40960
	v_mfma_f32_16x16x32_bf16 v[202:205], v[112:115], v[32:35], 0
	v_mfma_f32_16x16x32_bf16 v[206:209], v[116:119], v[32:35], 0
	ds_read_b128 v[236:239], v101 offset:32768
	ds_read_b128 v[240:243], v101 offset:40960
	v_max3_f32 v77, |v178|, |v179|, |v180|
	v_max3_f32 v84, |v186|, |v187|, |v188|
	v_mfma_f32_16x16x32_bf16 v[194:197], v[120:123], v[4:7], v[194:197]
	v_max3_f32 v78, |v181|, |v182|, |v183|
	v_max3_f32 v85, |v189|, |v190|, |v191|
	v_mfma_f32_16x16x32_bf16 v[198:201], v[124:127], v[4:7], v[198:201]
	v_max3_f32 v77, |v184|, |v185|, v77
	v_max3_f32 v84, |v192|, |v193|, v84
	v_mfma_f32_16x16x32_bf16 v[202:205], v[120:123], v[36:39], v[202:205]
	v_max_f32_e32 v77, v77, v78
	v_max_f32_e32 v84, v84, v85
	v_mfma_f32_16x16x32_bf16 v[206:209], v[124:127], v[36:39], v[206:209]
	ds_read_b128 v[112:115], v94 offset:32768
	ds_read_b128 v[116:119], v94 offset:40960
	v_mul_f32_e32 v77, 0x3c010204, v77
	v_mul_f32_e32 v84, 0x3c010204, v84
	v_mfma_f32_16x16x32_bf16 v[194:197], v[128:131], v[8:11], v[194:197]
	v_lshrrev_b32_e32 v79, 23, v77
	v_lshrrev_b32_e32 v110, 23, v84
	v_mfma_f32_16x16x32_bf16 v[198:201], v[132:135], v[8:11], v[198:201]
	v_and_b32_e32 v77, 0x7f800000, v77
	v_and_b32_e32 v84, 0x7f800000, v84
	v_mfma_f32_16x16x32_bf16 v[202:205], v[128:131], v[40:43], v[202:205]
	v_sub_u32_e32 v77, 0x7e800000, v77
	v_sub_u32_e32 v84, 0x7e800000, v84
	v_mfma_f32_16x16x32_bf16 v[206:209], v[132:135], v[40:43], v[206:209]
	ds_read_b128 v[120:123], v95 offset:32768
	ds_read_b128 v[124:127], v95 offset:40960
	v_fmaak_f32 v78, v178, v77, 0x43000000
	v_fmaak_f32 v85, v186, v84, 0x43000000
	v_mfma_f32_16x16x32_bf16 v[194:197], v[136:139], v[12:15], v[194:197]
	v_cvt_pk_u8_f32 v80, v78, 0, 0
	v_cvt_pk_u8_f32 v82, v85, 0, 0
	v_mfma_f32_16x16x32_bf16 v[198:201], v[140:143], v[12:15], v[198:201]
	v_fmaak_f32 v78, v179, v77, 0x43000000
	v_fmaak_f32 v85, v187, v84, 0x43000000
	v_mfma_f32_16x16x32_bf16 v[202:205], v[136:139], v[44:47], v[202:205]
	v_cvt_pk_u8_f32 v80, v78, 1, v80
	v_cvt_pk_u8_f32 v82, v85, 1, v82
	v_mfma_f32_16x16x32_bf16 v[206:209], v[140:143], v[44:47], v[206:209]
	ds_read_b128 v[128:131], v96 offset:32768
	ds_read_b128 v[132:135], v96 offset:40960
	v_fmaak_f32 v78, v180, v77, 0x43000000
	v_fmaak_f32 v85, v188, v84, 0x43000000
	v_mfma_f32_16x16x32_bf16 v[194:197], v[144:147], v[16:19], v[194:197]
	v_cvt_pk_u8_f32 v80, v78, 2, v80
	v_cvt_pk_u8_f32 v82, v85, 2, v82
	v_mfma_f32_16x16x32_bf16 v[198:201], v[148:151], v[16:19], v[198:201]
	v_fmaak_f32 v78, v181, v77, 0x43000000
	v_fmaak_f32 v85, v189, v84, 0x43000000
	v_mfma_f32_16x16x32_bf16 v[202:205], v[144:147], v[48:51], v[202:205]
	v_cvt_pk_u8_f32 v80, v78, 3, v80
	v_cvt_pk_u8_f32 v82, v85, 3, v82
	v_mfma_f32_16x16x32_bf16 v[206:209], v[148:151], v[48:51], v[206:209]
	ds_read_b128 v[136:139], v97 offset:32768
	ds_read_b128 v[140:143], v97 offset:40960
	v_fmaak_f32 v78, v182, v77, 0x43000000
	v_fmaak_f32 v85, v190, v84, 0x43000000
	v_mfma_f32_16x16x32_bf16 v[194:197], v[152:155], v[20:23], v[194:197]
	v_cvt_pk_u8_f32 v81, v78, 0, 0
	v_cvt_pk_u8_f32 v83, v85, 0, 0
	v_mfma_f32_16x16x32_bf16 v[198:201], v[156:159], v[20:23], v[198:201]
	v_fmaak_f32 v78, v183, v77, 0x43000000
	v_fmaak_f32 v85, v191, v84, 0x43000000
	v_mfma_f32_16x16x32_bf16 v[202:205], v[152:155], v[52:55], v[202:205]
	v_cvt_pk_u8_f32 v81, v78, 1, v81
	v_cvt_pk_u8_f32 v83, v85, 1, v83
	v_mfma_f32_16x16x32_bf16 v[206:209], v[156:159], v[52:55], v[206:209]
	ds_read_b128 v[144:147], v98 offset:32768
	ds_read_b128 v[148:151], v98 offset:40960
	v_fmaak_f32 v78, v184, v77, 0x43000000
	v_fmaak_f32 v85, v192, v84, 0x43000000
	v_mfma_f32_16x16x32_bf16 v[194:197], v[160:163], v[24:27], v[194:197]
	v_cvt_pk_u8_f32 v81, v78, 2, v81
	v_cvt_pk_u8_f32 v83, v85, 2, v83
	v_mfma_f32_16x16x32_bf16 v[198:201], v[164:167], v[24:27], v[198:201]
	v_fmaak_f32 v78, v185, v77, 0x43000000
	v_fmaak_f32 v85, v193, v84, 0x43000000
	v_mfma_f32_16x16x32_bf16 v[202:205], v[160:163], v[56:59], v[202:205]
	v_cvt_pk_u8_f32 v81, v78, 3, v81
	v_cvt_pk_u8_f32 v83, v85, 3, v83
	v_mfma_f32_16x16x32_bf16 v[206:209], v[164:167], v[56:59], v[206:209]
	ds_read_b128 v[152:155], v99 offset:32768
	ds_read_b128 v[156:159], v99 offset:40960
	v_add_u16_e32 v79, 1, v79
	v_add_u16_e32 v110, 1, v110
	v_mfma_f32_16x16x32_bf16 v[194:197], v[168:171], v[28:31], v[194:197]
	ds_write_b8 v106, v79 offset:128
	ds_write_b8 v106, v110 offset:2688
	v_mfma_f32_16x16x32_bf16 v[198:201], v[172:175], v[28:31], v[198:201]
	ds_write2st64_b64 v102, v[80:81], v[82:83] offset1:5
	v_mfma_f32_16x16x32_bf16 v[202:205], v[168:171], v[60:63], v[202:205]
	v_mfma_f32_16x16x32_bf16 v[206:209], v[172:175], v[60:63], v[206:209]
	s_waitcnt vmcnt(5) lgkmcnt(0)
	s_barrier
	v_mfma_f32_16x16x32_bf16 v[178:181], v[112:115], v[0:3], 0
	v_mfma_f32_16x16x32_bf16 v[182:185], v[116:119], v[0:3], 0
	ds_read_b128 v[160:163], v100 offset:49152
	ds_read_b128 v[164:167], v100 offset:57344
	v_mfma_f32_16x16x32_bf16 v[186:189], v[112:115], v[32:35], 0
	v_mfma_f32_16x16x32_bf16 v[190:193], v[116:119], v[32:35], 0
	ds_read_b128 v[168:171], v101 offset:49152
	ds_read_b128 v[172:175], v101 offset:57344
	v_max3_f32 v77, |v194|, |v195|, |v196|
	v_max3_f32 v84, |v202|, |v203|, |v204|
	v_mfma_f32_16x16x32_bf16 v[178:181], v[120:123], v[4:7], v[178:181]
	v_max3_f32 v78, |v197|, |v198|, |v199|
	v_max3_f32 v85, |v205|, |v206|, |v207|
	v_mfma_f32_16x16x32_bf16 v[182:185], v[124:127], v[4:7], v[182:185]
	v_max3_f32 v77, |v200|, |v201|, v77
	v_max3_f32 v84, |v208|, |v209|, v84
	v_mfma_f32_16x16x32_bf16 v[186:189], v[120:123], v[36:39], v[186:189]
	v_max_f32_e32 v77, v77, v78
	v_max_f32_e32 v84, v84, v85
	v_mfma_f32_16x16x32_bf16 v[190:193], v[124:127], v[36:39], v[190:193]
	ds_read_b128 v[112:115], v94 offset:49152
	ds_read_b128 v[116:119], v94 offset:57344
	v_mul_f32_e32 v77, 0x3c010204, v77
	v_mul_f32_e32 v84, 0x3c010204, v84
	v_mfma_f32_16x16x32_bf16 v[178:181], v[128:131], v[8:11], v[178:181]
	v_lshrrev_b32_e32 v79, 23, v77
	v_lshrrev_b32_e32 v110, 23, v84
	v_mfma_f32_16x16x32_bf16 v[182:185], v[132:135], v[8:11], v[182:185]
	v_and_b32_e32 v77, 0x7f800000, v77
	v_and_b32_e32 v84, 0x7f800000, v84
	v_mfma_f32_16x16x32_bf16 v[186:189], v[128:131], v[40:43], v[186:189]
	v_sub_u32_e32 v77, 0x7e800000, v77
	v_sub_u32_e32 v84, 0x7e800000, v84
	v_mfma_f32_16x16x32_bf16 v[190:193], v[132:135], v[40:43], v[190:193]
	ds_read_b128 v[120:123], v95 offset:49152
	ds_read_b128 v[124:127], v95 offset:57344
	v_fmaak_f32 v78, v194, v77, 0x43000000
	v_fmaak_f32 v85, v202, v84, 0x43000000
	v_mfma_f32_16x16x32_bf16 v[178:181], v[136:139], v[12:15], v[178:181]
	v_cvt_pk_u8_f32 v80, v78, 0, 0
	v_cvt_pk_u8_f32 v82, v85, 0, 0
	v_mfma_f32_16x16x32_bf16 v[182:185], v[140:143], v[12:15], v[182:185]
	v_fmaak_f32 v78, v195, v77, 0x43000000
	v_fmaak_f32 v85, v203, v84, 0x43000000
	v_mfma_f32_16x16x32_bf16 v[186:189], v[136:139], v[44:47], v[186:189]
	v_cvt_pk_u8_f32 v80, v78, 1, v80
	v_cvt_pk_u8_f32 v82, v85, 1, v82
	v_mfma_f32_16x16x32_bf16 v[190:193], v[140:143], v[44:47], v[190:193]
	ds_read_b128 v[128:131], v96 offset:49152
	ds_read_b128 v[132:135], v96 offset:57344
	v_fmaak_f32 v78, v196, v77, 0x43000000
	v_fmaak_f32 v85, v204, v84, 0x43000000
	v_mfma_f32_16x16x32_bf16 v[178:181], v[144:147], v[16:19], v[178:181]
	v_cvt_pk_u8_f32 v80, v78, 2, v80
	v_cvt_pk_u8_f32 v82, v85, 2, v82
	v_mfma_f32_16x16x32_bf16 v[182:185], v[148:151], v[16:19], v[182:185]
	v_fmaak_f32 v78, v197, v77, 0x43000000
	v_fmaak_f32 v85, v205, v84, 0x43000000
	v_mfma_f32_16x16x32_bf16 v[186:189], v[144:147], v[48:51], v[186:189]
	v_cvt_pk_u8_f32 v80, v78, 3, v80
	v_cvt_pk_u8_f32 v82, v85, 3, v82
	v_mfma_f32_16x16x32_bf16 v[190:193], v[148:151], v[48:51], v[190:193]
	ds_read_b128 v[136:139], v97 offset:49152
	ds_read_b128 v[140:143], v97 offset:57344
	v_fmaak_f32 v78, v198, v77, 0x43000000
	v_fmaak_f32 v85, v206, v84, 0x43000000
	v_mfma_f32_16x16x32_bf16 v[178:181], v[152:155], v[20:23], v[178:181]
	v_cvt_pk_u8_f32 v81, v78, 0, 0
	v_cvt_pk_u8_f32 v83, v85, 0, 0
	v_mfma_f32_16x16x32_bf16 v[182:185], v[156:159], v[20:23], v[182:185]
	v_fmaak_f32 v78, v199, v77, 0x43000000
	v_fmaak_f32 v85, v207, v84, 0x43000000
	v_mfma_f32_16x16x32_bf16 v[186:189], v[152:155], v[52:55], v[186:189]
	v_cvt_pk_u8_f32 v81, v78, 1, v81
	v_cvt_pk_u8_f32 v83, v85, 1, v83
	v_mfma_f32_16x16x32_bf16 v[190:193], v[156:159], v[52:55], v[190:193]
	ds_read_b128 v[144:147], v98 offset:49152
	ds_read_b128 v[148:151], v98 offset:57344
	v_fmaak_f32 v78, v200, v77, 0x43000000
	v_fmaak_f32 v85, v208, v84, 0x43000000
	v_mfma_f32_16x16x32_bf16 v[178:181], v[210:213], v[24:27], v[178:181]
	v_cvt_pk_u8_f32 v81, v78, 2, v81
	v_cvt_pk_u8_f32 v83, v85, 2, v83
	v_mfma_f32_16x16x32_bf16 v[182:185], v[214:217], v[24:27], v[182:185]
	v_fmaak_f32 v78, v201, v77, 0x43000000
	v_fmaak_f32 v85, v209, v84, 0x43000000
	v_mfma_f32_16x16x32_bf16 v[186:189], v[210:213], v[56:59], v[186:189]
	v_cvt_pk_u8_f32 v81, v78, 3, v81
	v_cvt_pk_u8_f32 v83, v85, 3, v83
	v_mfma_f32_16x16x32_bf16 v[190:193], v[214:217], v[56:59], v[190:193]
	ds_read_b128 v[152:155], v99 offset:49152
	ds_read_b128 v[156:159], v99 offset:57344
	v_add_u16_e32 v79, 1, v79
	v_add_u16_e32 v110, 1, v110
	v_mfma_f32_16x16x32_bf16 v[178:181], v[236:239], v[28:31], v[178:181]
	ds_write_b8 v106, v79 offset:132
	ds_write_b8 v106, v110 offset:2692
	v_mfma_f32_16x16x32_bf16 v[182:185], v[240:243], v[28:31], v[182:185]
	ds_write2st64_b64 v107, v[80:81], v[82:83] offset1:5
	v_mfma_f32_16x16x32_bf16 v[186:189], v[236:239], v[60:63], v[186:189]
	v_mfma_f32_16x16x32_bf16 v[190:193], v[240:243], v[60:63], v[190:193]
	s_waitcnt lgkmcnt(0)
	s_barrier
; DI void phase_edown3(const Ctx& c, int layer) {
;     ...
;         D2_BODY(0, 0, 0); D2_BODY(1, 1, 0);
; #pragma unroll 1
;         for (int J = 2; J < 16; J += 2) { D2_BODY(0, J, 5); D2_BODY(1, J + 1, 0); }
	v_mfma_f32_16x16x32_bf16 v[194:197], v[112:115], v[0:3], 0
	v_mfma_f32_16x16x32_bf16 v[198:201], v[116:119], v[0:3], 0
	v_mfma_f32_16x16x32_bf16 v[202:205], v[112:115], v[32:35], 0
	v_mfma_f32_16x16x32_bf16 v[206:209], v[116:119], v[32:35], 0
	v_max3_f32 v77, |v178|, |v179|, |v180|
	v_max3_f32 v84, |v186|, |v187|, |v188|
	v_mfma_f32_16x16x32_bf16 v[194:197], v[120:123], v[4:7], v[194:197]
	v_max3_f32 v78, |v181|, |v182|, |v183|
	v_max3_f32 v85, |v189|, |v190|, |v191|
	v_mfma_f32_16x16x32_bf16 v[198:201], v[124:127], v[4:7], v[198:201]
	v_max3_f32 v77, |v184|, |v185|, v77
	v_max3_f32 v84, |v192|, |v193|, v84
	v_mfma_f32_16x16x32_bf16 v[202:205], v[120:123], v[36:39], v[202:205]
	v_max_f32_e32 v77, v77, v78
	v_max_f32_e32 v84, v84, v85
	v_mfma_f32_16x16x32_bf16 v[206:209], v[124:127], v[36:39], v[206:209]
	v_mul_f32_e32 v77, 0x3c010204, v77
	v_mul_f32_e32 v84, 0x3c010204, v84
	v_mfma_f32_16x16x32_bf16 v[194:197], v[128:131], v[8:11], v[194:197]
	v_lshrrev_b32_e32 v79, 23, v77
	v_lshrrev_b32_e32 v110, 23, v84
	v_mfma_f32_16x16x32_bf16 v[198:201], v[132:135], v[8:11], v[198:201]
	v_and_b32_e32 v77, 0x7f800000, v77
	v_and_b32_e32 v84, 0x7f800000, v84
	v_mfma_f32_16x16x32_bf16 v[202:205], v[128:131], v[40:43], v[202:205]
	v_sub_u32_e32 v77, 0x7e800000, v77
	v_sub_u32_e32 v84, 0x7e800000, v84
	v_mfma_f32_16x16x32_bf16 v[206:209], v[132:135], v[40:43], v[206:209]
	v_fmaak_f32 v78, v178, v77, 0x43000000
	v_fmaak_f32 v85, v186, v84, 0x43000000
	v_mfma_f32_16x16x32_bf16 v[194:197], v[136:139], v[12:15], v[194:197]
	v_cvt_pk_u8_f32 v80, v78, 0, 0
	v_cvt_pk_u8_f32 v82, v85, 0, 0
	v_mfma_f32_16x16x32_bf16 v[198:201], v[140:143], v[12:15], v[198:201]
	v_fmaak_f32 v78, v179, v77, 0x43000000
	v_fmaak_f32 v85, v187, v84, 0x43000000
	v_mfma_f32_16x16x32_bf16 v[202:205], v[136:139], v[44:47], v[202:205]
	v_cvt_pk_u8_f32 v80, v78, 1, v80
	v_cvt_pk_u8_f32 v82, v85, 1, v82
	v_mfma_f32_16x16x32_bf16 v[206:209], v[140:143], v[44:47], v[206:209]
	v_fmaak_f32 v78, v180, v77, 0x43000000
	v_fmaak_f32 v85, v188, v84, 0x43000000
	v_mfma_f32_16x16x32_bf16 v[194:197], v[144:147], v[16:19], v[194:197]
	v_cvt_pk_u8_f32 v80, v78, 2, v80
	v_cvt_pk_u8_f32 v82, v85, 2, v82
	v_mfma_f32_16x16x32_bf16 v[198:201], v[148:151], v[16:19], v[198:201]
	v_fmaak_f32 v78, v181, v77, 0x43000000
	v_fmaak_f32 v85, v189, v84, 0x43000000
	v_mfma_f32_16x16x32_bf16 v[202:205], v[144:147], v[48:51], v[202:205]
	v_cvt_pk_u8_f32 v80, v78, 3, v80
	v_cvt_pk_u8_f32 v82, v85, 3, v82
	v_mfma_f32_16x16x32_bf16 v[206:209], v[148:151], v[48:51], v[206:209]
	v_fmaak_f32 v78, v182, v77, 0x43000000
	v_fmaak_f32 v85, v190, v84, 0x43000000
	v_mfma_f32_16x16x32_bf16 v[194:197], v[152:155], v[20:23], v[194:197]
	v_cvt_pk_u8_f32 v81, v78, 0, 0
	v_cvt_pk_u8_f32 v83, v85, 0, 0
	v_mfma_f32_16x16x32_bf16 v[198:201], v[156:159], v[20:23], v[198:201]
	v_fmaak_f32 v78, v183, v77, 0x43000000
	v_fmaak_f32 v85, v191, v84, 0x43000000
	v_mfma_f32_16x16x32_bf16 v[202:205], v[152:155], v[52:55], v[202:205]
	v_cvt_pk_u8_f32 v81, v78, 1, v81
	v_cvt_pk_u8_f32 v83, v85, 1, v83
	v_mfma_f32_16x16x32_bf16 v[206:209], v[156:159], v[52:55], v[206:209]
	v_fmaak_f32 v78, v184, v77, 0x43000000
	v_fmaak_f32 v85, v192, v84, 0x43000000
	v_mfma_f32_16x16x32_bf16 v[194:197], v[160:163], v[24:27], v[194:197]
	v_cvt_pk_u8_f32 v81, v78, 2, v81
	v_cvt_pk_u8_f32 v83, v85, 2, v83
	v_mfma_f32_16x16x32_bf16 v[198:201], v[164:167], v[24:27], v[198:201]
	v_fmaak_f32 v78, v185, v77, 0x43000000
	v_fmaak_f32 v85, v193, v84, 0x43000000
	v_mfma_f32_16x16x32_bf16 v[202:205], v[160:163], v[56:59], v[202:205]
	v_cvt_pk_u8_f32 v81, v78, 3, v81
	v_cvt_pk_u8_f32 v83, v85, 3, v83
	v_mfma_f32_16x16x32_bf16 v[206:209], v[164:167], v[56:59], v[206:209]
	v_add_u16_e32 v79, 1, v79
	v_add_u16_e32 v110, 1, v110
	v_mfma_f32_16x16x32_bf16 v[194:197], v[168:171], v[28:31], v[194:197]
	ds_write_b8 v106, v79 offset:136
	ds_write_b8 v106, v110 offset:2696
	v_mfma_f32_16x16x32_bf16 v[198:201], v[172:175], v[28:31], v[198:201]
	ds_write2st64_b64 v108, v[80:81], v[82:83] offset1:5
	v_mfma_f32_16x16x32_bf16 v[202:205], v[168:171], v[60:63], v[202:205]
	v_mfma_f32_16x16x32_bf16 v[206:209], v[172:175], v[60:63], v[206:209]
	s_nop 7
	v_max3_f32 v77, |v194|, |v195|, |v196|
	v_max3_f32 v84, |v202|, |v203|, |v204|
	v_max3_f32 v78, |v197|, |v198|, |v199|
	v_max3_f32 v85, |v205|, |v206|, |v207|
	v_max3_f32 v77, |v200|, |v201|, v77
	v_max3_f32 v84, |v208|, |v209|, v84
	v_max_f32_e32 v77, v77, v78
	v_max_f32_e32 v84, v84, v85
	v_mul_f32_e32 v77, 0x3c010204, v77
	v_mul_f32_e32 v84, 0x3c010204, v84
	v_lshrrev_b32_e32 v79, 23, v77
	v_lshrrev_b32_e32 v110, 23, v84
	v_and_b32_e32 v77, 0x7f800000, v77
	v_and_b32_e32 v84, 0x7f800000, v84
	v_sub_u32_e32 v77, 0x7e800000, v77
	v_sub_u32_e32 v84, 0x7e800000, v84
	v_fmaak_f32 v78, v194, v77, 0x43000000
	v_fmaak_f32 v85, v202, v84, 0x43000000
	v_cvt_pk_u8_f32 v80, v78, 0, 0
	v_cvt_pk_u8_f32 v82, v85, 0, 0
	v_fmaak_f32 v78, v195, v77, 0x43000000
	v_fmaak_f32 v85, v203, v84, 0x43000000
	v_cvt_pk_u8_f32 v80, v78, 1, v80
	v_cvt_pk_u8_f32 v82, v85, 1, v82
	v_fmaak_f32 v78, v196, v77, 0x43000000
	v_fmaak_f32 v85, v204, v84, 0x43000000
	v_cvt_pk_u8_f32 v80, v78, 2, v80
	v_cvt_pk_u8_f32 v82, v85, 2, v82
	v_fmaak_f32 v78, v197, v77, 0x43000000
	v_fmaak_f32 v85, v205, v84, 0x43000000
	v_cvt_pk_u8_f32 v80, v78, 3, v80
	v_cvt_pk_u8_f32 v82, v85, 3, v82
	v_fmaak_f32 v78, v198, v77, 0x43000000
	v_fmaak_f32 v85, v206, v84, 0x43000000
	v_cvt_pk_u8_f32 v81, v78, 0, 0
	v_cvt_pk_u8_f32 v83, v85, 0, 0
	v_fmaak_f32 v78, v199, v77, 0x43000000
	v_fmaak_f32 v85, v207, v84, 0x43000000
	v_cvt_pk_u8_f32 v81, v78, 1, v81
	v_cvt_pk_u8_f32 v83, v85, 1, v83
	v_fmaak_f32 v78, v200, v77, 0x43000000
	v_fmaak_f32 v85, v208, v84, 0x43000000
	v_cvt_pk_u8_f32 v81, v78, 2, v81
	v_cvt_pk_u8_f32 v83, v85, 2, v83
	v_fmaak_f32 v78, v201, v77, 0x43000000
	v_fmaak_f32 v85, v209, v84, 0x43000000
	v_cvt_pk_u8_f32 v81, v78, 3, v81
	v_cvt_pk_u8_f32 v83, v85, 3, v83
	v_add_u16_e32 v79, 1, v79
	v_add_u16_e32 v110, 1, v110
	ds_write_b8 v106, v79 offset:140
	ds_write_b8 v106, v110 offset:2700
	ds_write2st64_b64 v109, v[80:81], v[82:83] offset1:5
	s_waitcnt lgkmcnt(0)
	ds_read_b128 v[178:181], v103
	ds_read_b128 v[182:185], v103 offset:1280
	ds_read_b128 v[186:189], v103 offset:2560
	ds_read_b128 v[190:193], v103 offset:3840
	ds_read_b128 v[244:247], v104 offset:128
	s_waitcnt lgkmcnt(0)
	global_store_dwordx4 v72, v[178:181], s[10:11]
	global_store_dwordx4 v73, v[182:185], s[10:11]
	global_store_dwordx4 v74, v[186:189], s[10:11]
	global_store_dwordx4 v75, v[190:193], s[10:11]
	s_and_saveexec_b64 s[8:9], s[2:3]
	global_store_dwordx4 v76, v[244:247], s[10:11]
	s_or_b64 exec, exec, s[8:9]
	v_add_u32_e32 v72, 0x80, v72
	v_add_u32_e32 v73, 0x80, v73
	v_add_u32_e32 v74, 0x80, v74
	v_add_u32_e32 v75, 0x80, v75
	v_add_u32_e32 v76, 16, v76
	s_branch .LBB0_1256
